# removed 68 provably satisfied lgkmcnt waits inside the MFMA segments of the four GEMM K-loops (counter already zero after the pre-barrier lgkmcnt(0))
# speedup vs baseline: 1.0114x; 1.0041x over previous
; #define LAS __attribute__((address_space(3)))
;     __device__ __forceinline__ void a_offs_idx(const Unit& u, const unsigned (&nat)[2], unsigned (&v)[4], const LAS int*) const { a_offs(u, nat, v); }
; #define PG8_STAGE_A(bufoff, gbase, h) do { _Pragma("unroll") for (int _i = 0; _i < 2; ++_i) PG8_GLDS(gbase, va[(h) * 2 + _i], ldsb + (bufoff) + ldsw + _i * 8192); } while (0)
; #define PG8_STAGE_B(bufoff, gbase) do { _Pragma("unroll") for (int _i = 0; _i < 2; ++_i) PG8_GLDS(gbase, voffB[_i], ldsb + (bufoff) + ldsw + _i * 8192); } while (0)
; #define PG8_LDA(dst, b, h) do { _Pragma("unroll") for (int m = 0; m < 4; ++m) _Pragma("unroll") for (int k = 0; k < 2; ++k) dst[m][k] = *(const LAS i32x4*)(lds + PG8_SA(b, h) + aoff + m * 2048 + k * 1024); } while (0)
; #define PG8_LDB(dst, b, h) do { _Pragma("unroll") for (int n = 0; n < 2; ++n) _Pragma("unroll") for (int k = 0; k < 2; ++k) dst[n][k] = *(const LAS i32x4*)(lds + PG8_SB(b, h) + boff + n * 2048 + k * 1024); } while (0)
; #define PG8_WAIT_V(n) asm volatile("s_waitcnt vmcnt(" #n ")" ::: "memory")
; #define PG8_WAIT_L(n) asm volatile("s_waitcnt lgkmcnt(" #n ")" ::: "memory")
; template <class Epi, class Sched>
; __device__ __forceinline__ void gemm_phase(LAS unsigned char* lds, const Sched& S, const Epi& E) {
;     ...
;             PG8_LDB(B0, 0, 0); PG8_LDB(B1, 0, 1); PG8_SCHED; PG8_LDA(At, 0, 0); PG8_STAGE_A(PG8_SA(1, 1), a1, 1);
;             PG8_WAIT_V(8); PG8_WAIT_L(0); PG8_BAR; PG8_MMA(0, 0, At, B0); PG8_MMA(0, 1, At, B1); PG8_BAR; PG8_SCHED;
;             if (last && has_next) S.a_offs_idx(nxt, natA, va, (const LAS int*)(lds + IDX_OFF));
;             PG8_LDA(At, 0, 1); PG8_STAGE_B(PG8_SB(0, 0), b2); PG8_STAGE_B(PG8_SB(0, 1), b2 + HSTEP); PG8_STAGE_A(PG8_SA(0, 0), a2, 0);
;             PG8_WAIT_V(8); PG8_WAIT_L(0); PG8_BAR; PG8_MMA(1, 0, At, B0); PG8_MMA(1, 1, At, B1); PG8_BAR; PG8_SCHED;
;             PG8_LDB(B0, 1, 0); PG8_LDB(B1, 1, 1); PG8_SCHED; PG8_LDA(At, 1, 0); PG8_STAGE_A(PG8_SA(0, 1), a2, 1);
;             PG8_WAIT_V(8); PG8_WAIT_L(0); PG8_BAR; PG8_MMA(0, 0, At, B0); PG8_MMA(0, 1, At, B1); PG8_BAR; PG8_SCHED;
;             PG8_LDA(At, 1, 1); PG8_STAGE_B(PG8_SB(1, 0), b3); PG8_STAGE_B(PG8_SB(1, 1), b3 + HSTEP); PG8_STAGE_A(PG8_SA(1, 0), a3, 0);
;             PG8_WAIT_V(8); PG8_WAIT_L(0); PG8_BAR; PG8_MMA(1, 0, At, B0); PG8_MMA(1, 1, At, B1); PG8_BAR; PG8_SCHED;
.LBB0_212:
	s_add_u32 s56, s54, 0x100
	v_add_u32_e32 v158, 0x10000, v148
	v_add_u32_e32 v174, 0x14000, v148
	s_addc_u32 s57, s55, 0
	ds_read_b128 v[136:139], v158
	ds_read_b128 v[150:153], v158 offset:1024
	ds_read_b128 v[154:157], v158 offset:2048
	ds_read_b128 v[158:161], v158 offset:3072
	ds_read_b128 v[162:165], v174
	ds_read_b128 v[166:169], v174 offset:1024
	ds_read_b128 v[170:173], v174 offset:2048
	ds_read_b128 v[174:177], v174 offset:3072
	s_cmp_eq_u32 vcc_lo, 28
	s_cselect_b32 s80, s25, s56
	s_cselect_b32 s81, s23, s57
	s_cselect_b32 s78, s39, s66
	s_cselect_b32 s79, s21, s67
	s_add_u32 s76, s80, 0x80
	s_addc_u32 s77, s81, 0
	s_add_u32 s54, s54, 0x80
	s_addc_u32 s55, s55, 0
	ds_read_b128 v[178:181], v149
	ds_read_b128 v[182:185], v149 offset:1024
	ds_read_b128 v[186:189], v149 offset:2048
	ds_read_b128 v[190:193], v149 offset:3072
	ds_read_b128 v[194:197], v149 offset:4096
	ds_read_b128 v[198:201], v149 offset:5120
	ds_read_b128 v[202:205], v149 offset:6144
	ds_read_b128 v[206:209], v149 offset:7168
	s_mov_b32 s12, m0
	s_mov_b32 m0, s64
	s_nop 0
	global_load_lds_dwordx4 v146, s[54:55]
	s_mov_b32 m0, s12
	s_nop 0
	s_mov_b32 s12, m0
	s_mov_b32 m0, s65
	s_nop 0
	global_load_lds_dwordx4 v147, s[54:55]
	s_mov_b32 m0, s12
	s_waitcnt vmcnt(8)
	s_waitcnt lgkmcnt(0)
	s_barrier
	s_setprio 1
	v_mfma_f32_16x16x32_bf16 v[126:129], v[136:139], v[178:181], v[126:129]
	v_mfma_f32_16x16x32_bf16 v[122:125], v[154:157], v[178:181], v[122:125]
	v_mfma_f32_16x16x32_bf16 v[118:121], v[136:139], v[186:189], v[118:121]
	v_mfma_f32_16x16x32_bf16 v[114:117], v[154:157], v[186:189], v[114:117]
	v_mfma_f32_16x16x32_bf16 v[102:105], v[136:139], v[194:197], v[102:105]
	v_mfma_f32_16x16x32_bf16 v[98:101], v[154:157], v[194:197], v[98:101]
	v_mfma_f32_16x16x32_bf16 v[86:89], v[136:139], v[202:205], v[86:89]
	v_mfma_f32_16x16x32_bf16 v[82:85], v[154:157], v[202:205], v[82:85]
	v_mfma_f32_16x16x32_bf16 v[126:129], v[150:153], v[182:185], v[126:129]
	v_mfma_f32_16x16x32_bf16 v[122:125], v[158:161], v[182:185], v[122:125]
	v_mfma_f32_16x16x32_bf16 v[118:121], v[150:153], v[190:193], v[118:121]
	v_mfma_f32_16x16x32_bf16 v[114:117], v[158:161], v[190:193], v[114:117]
	v_mfma_f32_16x16x32_bf16 v[102:105], v[150:153], v[198:201], v[102:105]
	v_mfma_f32_16x16x32_bf16 v[98:101], v[158:161], v[198:201], v[98:101]
	v_mfma_f32_16x16x32_bf16 v[86:89], v[150:153], v[206:209], v[86:89]
	v_mfma_f32_16x16x32_bf16 v[82:85], v[158:161], v[206:209], v[82:85]
	s_setprio 0
	s_setprio 1
	v_mfma_f32_16x16x32_bf16 v[110:113], v[162:165], v[178:181], v[110:113]
	s_add_u32 s54, s78, 0x80
	s_addc_u32 s55, s79, 0
	v_mfma_f32_16x16x32_bf16 v[106:109], v[170:173], v[178:181], v[106:109]
	v_mfma_f32_16x16x32_bf16 v[94:97], v[162:165], v[186:189], v[94:97]
	v_mfma_f32_16x16x32_bf16 v[90:93], v[170:173], v[186:189], v[90:93]
	v_mfma_f32_16x16x32_bf16 v[78:81], v[162:165], v[194:197], v[78:81]
	v_mfma_f32_16x16x32_bf16 v[74:77], v[170:173], v[194:197], v[74:77]
	v_mfma_f32_16x16x32_bf16 v[70:73], v[162:165], v[202:205], v[70:73]
	v_mfma_f32_16x16x32_bf16 v[66:69], v[170:173], v[202:205], v[66:69]
	v_mfma_f32_16x16x32_bf16 v[110:113], v[166:169], v[182:185], v[110:113]
	v_mfma_f32_16x16x32_bf16 v[106:109], v[174:177], v[182:185], v[106:109]
	v_mfma_f32_16x16x32_bf16 v[94:97], v[166:169], v[190:193], v[94:97]
	v_mfma_f32_16x16x32_bf16 v[90:93], v[174:177], v[190:193], v[90:93]
	v_mfma_f32_16x16x32_bf16 v[78:81], v[166:169], v[198:201], v[78:81]
	v_mfma_f32_16x16x32_bf16 v[74:77], v[174:177], v[198:201], v[74:77]
	v_mfma_f32_16x16x32_bf16 v[70:73], v[166:169], v[206:209], v[70:73]
	v_mfma_f32_16x16x32_bf16 v[66:69], v[174:177], v[206:209], v[66:69]
	s_setprio 0
	s_barrier
	ds_read_b128 v[178:181], v149 offset:16384
	ds_read_b128 v[182:185], v149 offset:17408
	ds_read_b128 v[186:189], v149 offset:18432
	ds_read_b128 v[190:193], v149 offset:19456
	ds_read_b128 v[194:197], v149 offset:20480
	ds_read_b128 v[198:201], v149 offset:21504
	ds_read_b128 v[202:205], v149 offset:22528
	ds_read_b128 v[206:209], v149 offset:23552
	s_mov_b32 s12, m0
	s_mov_b32 m0, s96
	s_nop 0
	global_load_lds_dwordx4 v143, s[78:79]
	s_mov_b32 m0, s12
	s_nop 0
	s_mov_b32 s12, m0
	s_mov_b32 m0, s95
	s_nop 0
	global_load_lds_dwordx4 v145, s[78:79]
	s_mov_b32 m0, s12
	s_add_u32 s12, s78, 0x80000
	s_addc_u32 s13, s79, 0
	s_mov_b32 vcc_hi, m0
	s_mov_b32 m0, s30
	s_nop 0
	global_load_lds_dwordx4 v143, s[12:13]
	s_mov_b32 m0, vcc_hi
	s_nop 0
	s_mov_b32 vcc_hi, m0
	s_mov_b32 m0, s31
	s_nop 0
	global_load_lds_dwordx4 v145, s[12:13]
	s_mov_b32 m0, vcc_hi
	s_mov_b32 s12, m0
	s_mov_b32 m0, s84
	s_nop 0
	global_load_lds_dwordx4 v130, s[80:81]
	s_mov_b32 m0, s12
	s_nop 0
	s_mov_b32 s12, m0
	s_mov_b32 m0, s2
	s_nop 0
	global_load_lds_dwordx4 v144, s[80:81]
	s_mov_b32 m0, s12
	s_waitcnt vmcnt(8)
	s_waitcnt lgkmcnt(0)
	s_barrier
; #define LAS __attribute__((address_space(3)))
;     __device__ __forceinline__ void a_offs_idx(const Unit& u, const unsigned (&nat)[2], unsigned (&v)[4], const LAS int*) const { a_offs(u, nat, v); }
; #define PG8_STAGE_A(bufoff, gbase, h) do { _Pragma("unroll") for (int _i = 0; _i < 2; ++_i) PG8_GLDS(gbase, va[(h) * 2 + _i], ldsb + (bufoff) + ldsw + _i * 8192); } while (0)
; #define PG8_STAGE_B(bufoff, gbase) do { _Pragma("unroll") for (int _i = 0; _i < 2; ++_i) PG8_GLDS(gbase, voffB[_i], ldsb + (bufoff) + ldsw + _i * 8192); } while (0)
; #define PG8_LDA(dst, b, h) do { _Pragma("unroll") for (int m = 0; m < 4; ++m) _Pragma("unroll") for (int k = 0; k < 2; ++k) dst[m][k] = *(const LAS i32x4*)(lds + PG8_SA(b, h) + aoff + m * 2048 + k * 1024); } while (0)
; #define PG8_LDB(dst, b, h) do { _Pragma("unroll") for (int n = 0; n < 2; ++n) _Pragma("unroll") for (int k = 0; k < 2; ++k) dst[n][k] = *(const LAS i32x4*)(lds + PG8_SB(b, h) + boff + n * 2048 + k * 1024); } while (0)
; #define PG8_WAIT_V(n) asm volatile("s_waitcnt vmcnt(" #n ")" ::: "memory")
; #define PG8_WAIT_L(n) asm volatile("s_waitcnt lgkmcnt(" #n ")" ::: "memory")
; template <class Epi, class Sched>
; __device__ __forceinline__ void gemm_phase(LAS unsigned char* lds, const Sched& S, const Epi& E) {
;     ...
;             PG8_LDB(B0, 0, 0); PG8_LDB(B1, 0, 1); PG8_SCHED; PG8_LDA(At, 0, 0); PG8_STAGE_A(PG8_SA(1, 1), a1, 1);
;             PG8_WAIT_V(8); PG8_WAIT_L(0); PG8_BAR; PG8_MMA(0, 0, At, B0); PG8_MMA(0, 1, At, B1); PG8_BAR; PG8_SCHED;
;             if (last && has_next) S.a_offs_idx(nxt, natA, va, (const LAS int*)(lds + IDX_OFF));
;             PG8_LDA(At, 0, 1); PG8_STAGE_B(PG8_SB(0, 0), b2); PG8_STAGE_B(PG8_SB(0, 1), b2 + HSTEP); PG8_STAGE_A(PG8_SA(0, 0), a2, 0);
;             PG8_WAIT_V(8); PG8_WAIT_L(0); PG8_BAR; PG8_MMA(1, 0, At, B0); PG8_MMA(1, 1, At, B1); PG8_BAR; PG8_SCHED;
;             PG8_LDB(B0, 1, 0); PG8_LDB(B1, 1, 1); PG8_SCHED; PG8_LDA(At, 1, 0); PG8_STAGE_A(PG8_SA(0, 1), a2, 1);
;             PG8_WAIT_V(8); PG8_WAIT_L(0); PG8_BAR; PG8_MMA(0, 0, At, B0); PG8_MMA(0, 1, At, B1); PG8_BAR; PG8_SCHED;
;             PG8_LDA(At, 1, 1); PG8_STAGE_B(PG8_SB(1, 0), b3); PG8_STAGE_B(PG8_SB(1, 1), b3 + HSTEP); PG8_STAGE_A(PG8_SA(1, 0), a3, 0);
;             PG8_WAIT_V(8); PG8_WAIT_L(0); PG8_BAR; PG8_MMA(1, 0, At, B0); PG8_MMA(1, 1, At, B1); PG8_BAR; PG8_SCHED;
	s_setprio 1
	v_mfma_f32_16x16x32_bf16 v[62:65], v[136:139], v[178:181], v[62:65]
	v_mfma_f32_16x16x32_bf16 v[58:61], v[154:157], v[178:181], v[58:61]
	v_mfma_f32_16x16x32_bf16 v[54:57], v[136:139], v[186:189], v[54:57]
	v_mfma_f32_16x16x32_bf16 v[50:53], v[154:157], v[186:189], v[50:53]
	v_mfma_f32_16x16x32_bf16 v[38:41], v[136:139], v[194:197], v[38:41]
	v_mfma_f32_16x16x32_bf16 v[34:37], v[154:157], v[194:197], v[34:37]
	v_mfma_f32_16x16x32_bf16 v[22:25], v[136:139], v[202:205], v[22:25]
	v_mfma_f32_16x16x32_bf16 v[18:21], v[154:157], v[202:205], v[18:21]
	v_mfma_f32_16x16x32_bf16 v[62:65], v[150:153], v[182:185], v[62:65]
	v_mfma_f32_16x16x32_bf16 v[58:61], v[158:161], v[182:185], v[58:61]
	v_mfma_f32_16x16x32_bf16 v[54:57], v[150:153], v[190:193], v[54:57]
	v_mfma_f32_16x16x32_bf16 v[50:53], v[158:161], v[190:193], v[50:53]
	v_mfma_f32_16x16x32_bf16 v[38:41], v[150:153], v[198:201], v[38:41]
	v_mfma_f32_16x16x32_bf16 v[34:37], v[158:161], v[198:201], v[34:37]
	v_mfma_f32_16x16x32_bf16 v[22:25], v[150:153], v[206:209], v[22:25]
	v_mfma_f32_16x16x32_bf16 v[18:21], v[158:161], v[206:209], v[18:21]
	s_setprio 0
	s_setprio 1
	v_mfma_f32_16x16x32_bf16 v[46:49], v[162:165], v[178:181], v[46:49]
	v_mfma_f32_16x16x32_bf16 v[42:45], v[170:173], v[178:181], v[42:45]
	v_mfma_f32_16x16x32_bf16 v[30:33], v[162:165], v[186:189], v[30:33]
	v_mfma_f32_16x16x32_bf16 v[26:29], v[170:173], v[186:189], v[26:29]
	v_mfma_f32_16x16x32_bf16 v[14:17], v[162:165], v[194:197], v[14:17]
	v_mfma_f32_16x16x32_bf16 v[10:13], v[170:173], v[194:197], v[10:13]
	v_mfma_f32_16x16x32_bf16 v[6:9], v[162:165], v[202:205], v[6:9]
	v_mfma_f32_16x16x32_bf16 v[2:5], v[170:173], v[202:205], v[2:5]
	v_mfma_f32_16x16x32_bf16 v[46:49], v[166:169], v[182:185], v[46:49]
	v_mfma_f32_16x16x32_bf16 v[42:45], v[174:177], v[182:185], v[42:45]
	v_mfma_f32_16x16x32_bf16 v[30:33], v[166:169], v[190:193], v[30:33]
	v_mfma_f32_16x16x32_bf16 v[26:29], v[174:177], v[190:193], v[26:29]
	v_mfma_f32_16x16x32_bf16 v[14:17], v[166:169], v[198:201], v[14:17]
	v_mfma_f32_16x16x32_bf16 v[10:13], v[174:177], v[198:201], v[10:13]
	v_mfma_f32_16x16x32_bf16 v[6:9], v[166:169], v[206:209], v[6:9]
	v_mfma_f32_16x16x32_bf16 v[2:5], v[174:177], v[206:209], v[2:5]
	s_setprio 0
	s_barrier
	v_add_u32_e32 v158, 0x18000, v148
	v_add_u32_e32 v174, 0x1c000, v148
	ds_read_b128 v[136:139], v158
	ds_read_b128 v[150:153], v158 offset:1024
	ds_read_b128 v[154:157], v158 offset:2048
	ds_read_b128 v[158:161], v158 offset:3072
	ds_read_b128 v[162:165], v174
	ds_read_b128 v[166:169], v174 offset:1024
	ds_read_b128 v[170:173], v174 offset:2048
	ds_read_b128 v[174:177], v174 offset:3072
	ds_read_b128 v[178:181], v149 offset:32768
	ds_read_b128 v[182:185], v149 offset:33792
	ds_read_b128 v[186:189], v149 offset:34816
	ds_read_b128 v[190:193], v149 offset:35840
	ds_read_b128 v[194:197], v149 offset:36864
	ds_read_b128 v[198:201], v149 offset:37888
	ds_read_b128 v[202:205], v149 offset:38912
	ds_read_b128 v[206:209], v149 offset:39936
	s_mov_b32 s12, m0
	s_mov_b32 m0, s83
	s_nop 0
	global_load_lds_dwordx4 v146, s[80:81]
	s_mov_b32 m0, s12
	s_nop 0
	s_mov_b32 s12, m0
	s_mov_b32 m0, s87
	s_nop 0
	global_load_lds_dwordx4 v147, s[80:81]
	s_mov_b32 m0, s12
	s_waitcnt vmcnt(8)
	s_waitcnt lgkmcnt(0)
	s_barrier
	s_setprio 1
	v_mfma_f32_16x16x32_bf16 v[126:129], v[136:139], v[178:181], v[126:129]
	v_mfma_f32_16x16x32_bf16 v[122:125], v[154:157], v[178:181], v[122:125]
	v_mfma_f32_16x16x32_bf16 v[118:121], v[136:139], v[186:189], v[118:121]
	v_mfma_f32_16x16x32_bf16 v[114:117], v[154:157], v[186:189], v[114:117]
	v_mfma_f32_16x16x32_bf16 v[102:105], v[136:139], v[194:197], v[102:105]
	v_mfma_f32_16x16x32_bf16 v[98:101], v[154:157], v[194:197], v[98:101]
	v_mfma_f32_16x16x32_bf16 v[86:89], v[136:139], v[202:205], v[86:89]
	v_mfma_f32_16x16x32_bf16 v[82:85], v[154:157], v[202:205], v[82:85]
	v_mfma_f32_16x16x32_bf16 v[126:129], v[150:153], v[182:185], v[126:129]
	v_mfma_f32_16x16x32_bf16 v[122:125], v[158:161], v[182:185], v[122:125]
	v_mfma_f32_16x16x32_bf16 v[118:121], v[150:153], v[190:193], v[118:121]
	v_mfma_f32_16x16x32_bf16 v[114:117], v[158:161], v[190:193], v[114:117]
	v_mfma_f32_16x16x32_bf16 v[102:105], v[150:153], v[198:201], v[102:105]
	v_mfma_f32_16x16x32_bf16 v[98:101], v[158:161], v[198:201], v[98:101]
	v_mfma_f32_16x16x32_bf16 v[86:89], v[150:153], v[206:209], v[86:89]
	v_mfma_f32_16x16x32_bf16 v[82:85], v[158:161], v[206:209], v[82:85]
	s_setprio 0
	s_setprio 1
	v_mfma_f32_16x16x32_bf16 v[110:113], v[162:165], v[178:181], v[110:113]
	v_mfma_f32_16x16x32_bf16 v[106:109], v[170:173], v[178:181], v[106:109]
	v_mfma_f32_16x16x32_bf16 v[94:97], v[162:165], v[186:189], v[94:97]
	v_mfma_f32_16x16x32_bf16 v[90:93], v[170:173], v[186:189], v[90:93]
	v_mfma_f32_16x16x32_bf16 v[78:81], v[162:165], v[194:197], v[78:81]
	v_mfma_f32_16x16x32_bf16 v[74:77], v[170:173], v[194:197], v[74:77]
	v_mfma_f32_16x16x32_bf16 v[70:73], v[162:165], v[202:205], v[70:73]
	v_mfma_f32_16x16x32_bf16 v[66:69], v[170:173], v[202:205], v[66:69]
	v_mfma_f32_16x16x32_bf16 v[110:113], v[166:169], v[182:185], v[110:113]
	v_mfma_f32_16x16x32_bf16 v[106:109], v[174:177], v[182:185], v[106:109]
	v_mfma_f32_16x16x32_bf16 v[94:97], v[166:169], v[190:193], v[94:97]
	v_mfma_f32_16x16x32_bf16 v[90:93], v[174:177], v[190:193], v[90:93]
	v_mfma_f32_16x16x32_bf16 v[78:81], v[166:169], v[198:201], v[78:81]
	v_mfma_f32_16x16x32_bf16 v[74:77], v[174:177], v[198:201], v[74:77]
	v_mfma_f32_16x16x32_bf16 v[70:73], v[166:169], v[206:209], v[70:73]
	v_mfma_f32_16x16x32_bf16 v[66:69], v[174:177], v[206:209], v[66:69]
	s_setprio 0
	s_barrier
; #define LAS __attribute__((address_space(3)))
;     __device__ __forceinline__ void a_offs_idx(const Unit& u, const unsigned (&nat)[2], unsigned (&v)[4], const LAS int*) const { a_offs(u, nat, v); }
; #define PG8_STAGE_A(bufoff, gbase, h) do { _Pragma("unroll") for (int _i = 0; _i < 2; ++_i) PG8_GLDS(gbase, va[(h) * 2 + _i], ldsb + (bufoff) + ldsw + _i * 8192); } while (0)
; #define PG8_STAGE_B(bufoff, gbase) do { _Pragma("unroll") for (int _i = 0; _i < 2; ++_i) PG8_GLDS(gbase, voffB[_i], ldsb + (bufoff) + ldsw + _i * 8192); } while (0)
; #define PG8_LDA(dst, b, h) do { _Pragma("unroll") for (int m = 0; m < 4; ++m) _Pragma("unroll") for (int k = 0; k < 2; ++k) dst[m][k] = *(const LAS i32x4*)(lds + PG8_SA(b, h) + aoff + m * 2048 + k * 1024); } while (0)
; #define PG8_LDB(dst, b, h) do { _Pragma("unroll") for (int n = 0; n < 2; ++n) _Pragma("unroll") for (int k = 0; k < 2; ++k) dst[n][k] = *(const LAS i32x4*)(lds + PG8_SB(b, h) + boff + n * 2048 + k * 1024); } while (0)
; #define PG8_WAIT_V(n) asm volatile("s_waitcnt vmcnt(" #n ")" ::: "memory")
; #define PG8_WAIT_L(n) asm volatile("s_waitcnt lgkmcnt(" #n ")" ::: "memory")
; template <class Epi, class Sched>
; __device__ __forceinline__ void gemm_phase(LAS unsigned char* lds, const Sched& S, const Epi& E) {
;     ...
;             PG8_LDB(B0, 0, 0); PG8_LDB(B1, 0, 1); PG8_SCHED; PG8_LDA(At, 0, 0); PG8_STAGE_A(PG8_SA(1, 1), a1, 1);
;             PG8_WAIT_V(8); PG8_WAIT_L(0); PG8_BAR; PG8_MMA(0, 0, At, B0); PG8_MMA(0, 1, At, B1); PG8_BAR; PG8_SCHED;
;             if (last && has_next) S.a_offs_idx(nxt, natA, va, (const LAS int*)(lds + IDX_OFF));
;             PG8_LDA(At, 0, 1); PG8_STAGE_B(PG8_SB(0, 0), b2); PG8_STAGE_B(PG8_SB(0, 1), b2 + HSTEP); PG8_STAGE_A(PG8_SA(0, 0), a2, 0);
;             PG8_WAIT_V(8); PG8_WAIT_L(0); PG8_BAR; PG8_MMA(1, 0, At, B0); PG8_MMA(1, 1, At, B1); PG8_BAR; PG8_SCHED;
;             PG8_LDB(B0, 1, 0); PG8_LDB(B1, 1, 1); PG8_SCHED; PG8_LDA(At, 1, 0); PG8_STAGE_A(PG8_SA(0, 1), a2, 1);
;             PG8_WAIT_V(8); PG8_WAIT_L(0); PG8_BAR; PG8_MMA(0, 0, At, B0); PG8_MMA(0, 1, At, B1); PG8_BAR; PG8_SCHED;
;             PG8_LDA(At, 1, 1); PG8_STAGE_B(PG8_SB(1, 0), b3); PG8_STAGE_B(PG8_SB(1, 1), b3 + HSTEP); PG8_STAGE_A(PG8_SA(1, 0), a3, 0);
;             PG8_WAIT_V(8); PG8_WAIT_L(0); PG8_BAR; PG8_MMA(1, 0, At, B0); PG8_MMA(1, 1, At, B1); PG8_BAR; PG8_SCHED;
	ds_read_b128 v[178:181], v149 offset:49152
	ds_read_b128 v[182:185], v149 offset:50176
	ds_read_b128 v[186:189], v149 offset:51200
	ds_read_b128 v[190:193], v149 offset:52224
	ds_read_b128 v[194:197], v149 offset:53248
	ds_read_b128 v[198:201], v149 offset:54272
	ds_read_b128 v[202:205], v149 offset:55296
	ds_read_b128 v[206:209], v149 offset:56320
	s_mov_b32 s12, m0
	s_mov_b32 m0, s58
	s_nop 0
	global_load_lds_dwordx4 v143, s[54:55]
	s_mov_b32 m0, s12
	s_nop 0
	s_mov_b32 s12, m0
	s_mov_b32 m0, s59
	s_nop 0
	global_load_lds_dwordx4 v145, s[54:55]
	s_mov_b32 m0, s12
	s_add_u32 s12, s78, 0x80080
	s_addc_u32 s13, s79, 0
	s_mov_b32 s54, m0
	s_mov_b32 m0, s62
	s_nop 0
	global_load_lds_dwordx4 v143, s[12:13]
	s_mov_b32 m0, s54
	s_nop 0
	s_mov_b32 s54, m0
	s_mov_b32 m0, s63
	s_nop 0
	global_load_lds_dwordx4 v145, s[12:13]
	s_mov_b32 m0, s54
	s_mov_b32 s12, m0
	s_mov_b32 m0, s60
	s_nop 0
	global_load_lds_dwordx4 v130, s[76:77]
	s_mov_b32 m0, s12
	s_nop 0
	s_mov_b32 s12, m0
	s_mov_b32 m0, s61
	s_nop 0
	global_load_lds_dwordx4 v144, s[76:77]
	s_mov_b32 m0, s12
	s_waitcnt vmcnt(8)
	s_waitcnt lgkmcnt(0)
	s_barrier
	s_setprio 1
	v_mfma_f32_16x16x32_bf16 v[62:65], v[136:139], v[178:181], v[62:65]
	v_mfma_f32_16x16x32_bf16 v[58:61], v[154:157], v[178:181], v[58:61]
	v_mfma_f32_16x16x32_bf16 v[54:57], v[136:139], v[186:189], v[54:57]
	v_mfma_f32_16x16x32_bf16 v[50:53], v[154:157], v[186:189], v[50:53]
	v_mfma_f32_16x16x32_bf16 v[38:41], v[136:139], v[194:197], v[38:41]
	v_mfma_f32_16x16x32_bf16 v[34:37], v[154:157], v[194:197], v[34:37]
	v_mfma_f32_16x16x32_bf16 v[22:25], v[136:139], v[202:205], v[22:25]
	v_mfma_f32_16x16x32_bf16 v[18:21], v[154:157], v[202:205], v[18:21]
	v_mfma_f32_16x16x32_bf16 v[62:65], v[150:153], v[182:185], v[62:65]
	v_mfma_f32_16x16x32_bf16 v[58:61], v[158:161], v[182:185], v[58:61]
	v_mfma_f32_16x16x32_bf16 v[54:57], v[150:153], v[190:193], v[54:57]
	v_mfma_f32_16x16x32_bf16 v[50:53], v[158:161], v[190:193], v[50:53]
	v_mfma_f32_16x16x32_bf16 v[38:41], v[150:153], v[198:201], v[38:41]
	v_mfma_f32_16x16x32_bf16 v[34:37], v[158:161], v[198:201], v[34:37]
	v_mfma_f32_16x16x32_bf16 v[22:25], v[150:153], v[206:209], v[22:25]
	v_mfma_f32_16x16x32_bf16 v[18:21], v[158:161], v[206:209], v[18:21]
	s_setprio 0
	s_setprio 1
	v_mfma_f32_16x16x32_bf16 v[46:49], v[162:165], v[178:181], v[46:49]
	v_mfma_f32_16x16x32_bf16 v[42:45], v[170:173], v[178:181], v[42:45]
	v_mfma_f32_16x16x32_bf16 v[30:33], v[162:165], v[186:189], v[30:33]
	v_mfma_f32_16x16x32_bf16 v[26:29], v[170:173], v[186:189], v[26:29]
	v_mfma_f32_16x16x32_bf16 v[14:17], v[162:165], v[194:197], v[14:17]
	v_mfma_f32_16x16x32_bf16 v[10:13], v[170:173], v[194:197], v[10:13]
	v_mfma_f32_16x16x32_bf16 v[6:9], v[162:165], v[202:205], v[6:9]
	v_mfma_f32_16x16x32_bf16 v[2:5], v[170:173], v[202:205], v[2:5]
	v_mfma_f32_16x16x32_bf16 v[46:49], v[166:169], v[182:185], v[46:49]
	v_mfma_f32_16x16x32_bf16 v[42:45], v[174:177], v[182:185], v[42:45]
	v_mfma_f32_16x16x32_bf16 v[30:33], v[166:169], v[190:193], v[30:33]
	v_mfma_f32_16x16x32_bf16 v[26:29], v[174:177], v[190:193], v[26:29]
	v_mfma_f32_16x16x32_bf16 v[14:17], v[166:169], v[198:201], v[14:17]
	v_mfma_f32_16x16x32_bf16 v[10:13], v[174:177], v[198:201], v[10:13]
	v_mfma_f32_16x16x32_bf16 v[6:9], v[166:169], v[206:209], v[6:9]
	v_mfma_f32_16x16x32_bf16 v[2:5], v[174:177], v[206:209], v[2:5]
	s_setprio 0
	s_barrier
	s_add_i32 vcc_lo, vcc_lo, 2
	s_add_u32 s66, s66, 0x100
	s_addc_u32 s67, s67, 0
	s_cmp_gt_u32 vcc_lo, 29
	s_mov_b64 s[54:55], s[56:57]
	s_cbranch_scc0 .LBB0_212
	s_and_b64 vcc, exec, s[16:17]
	s_cbranch_vccz .LBB0_215
	s_barrier

; #define LAS __attribute__((address_space(3)))
;     __device__ __forceinline__ void a_offs_idx(const Unit& u, const unsigned (&nat)[2], unsigned (&v)[4], const LAS int*) const { a_offs(u, nat, v); }
; #define PG8_STAGE_A(bufoff, gbase, h) do { _Pragma("unroll") for (int _i = 0; _i < 2; ++_i) PG8_GLDS(gbase, va[(h) * 2 + _i], ldsb + (bufoff) + ldsw + _i * 8192); } while (0)
; #define PG8_STAGE_B(bufoff, gbase) do { _Pragma("unroll") for (int _i = 0; _i < 2; ++_i) PG8_GLDS(gbase, voffB[_i], ldsb + (bufoff) + ldsw + _i * 8192); } while (0)
; #define PG8_LDA(dst, b, h) do { _Pragma("unroll") for (int m = 0; m < 4; ++m) _Pragma("unroll") for (int k = 0; k < 2; ++k) dst[m][k] = *(const LAS i32x4*)(lds + PG8_SA(b, h) + aoff + m * 2048 + k * 1024); } while (0)
; #define PG8_LDB(dst, b, h) do { _Pragma("unroll") for (int n = 0; n < 2; ++n) _Pragma("unroll") for (int k = 0; k < 2; ++k) dst[n][k] = *(const LAS i32x4*)(lds + PG8_SB(b, h) + boff + n * 2048 + k * 1024); } while (0)
; #define PG8_WAIT_V(n) asm volatile("s_waitcnt vmcnt(" #n ")" ::: "memory")
; #define PG8_WAIT_L(n) asm volatile("s_waitcnt lgkmcnt(" #n ")" ::: "memory")
; template <class Epi, class Sched>
; __device__ __forceinline__ void gemm_phase(LAS unsigned char* lds, const Sched& S, const Epi& E) {
;     ...
;             PG8_LDB(B0, 0, 0); PG8_LDB(B1, 0, 1); PG8_SCHED; PG8_LDA(At, 0, 0); PG8_STAGE_A(PG8_SA(1, 1), a1, 1);
;             PG8_WAIT_V(8); PG8_WAIT_L(0); PG8_BAR; PG8_MMA(0, 0, At, B0); PG8_MMA(0, 1, At, B1); PG8_BAR; PG8_SCHED;
;             if (last && has_next) S.a_offs_idx(nxt, natA, va, (const LAS int*)(lds + IDX_OFF));
;             PG8_LDA(At, 0, 1); PG8_STAGE_B(PG8_SB(0, 0), b2); PG8_STAGE_B(PG8_SB(0, 1), b2 + HSTEP); PG8_STAGE_A(PG8_SA(0, 0), a2, 0);
;             PG8_WAIT_V(8); PG8_WAIT_L(0); PG8_BAR; PG8_MMA(1, 0, At, B0); PG8_MMA(1, 1, At, B1); PG8_BAR; PG8_SCHED;
;             PG8_LDB(B0, 1, 0); PG8_LDB(B1, 1, 1); PG8_SCHED; PG8_LDA(At, 1, 0); PG8_STAGE_A(PG8_SA(0, 1), a2, 1);
;             PG8_WAIT_V(8); PG8_WAIT_L(0); PG8_BAR; PG8_MMA(0, 0, At, B0); PG8_MMA(0, 1, At, B1); PG8_BAR; PG8_SCHED;
;             PG8_LDA(At, 1, 1); PG8_STAGE_B(PG8_SB(1, 0), b3); PG8_STAGE_B(PG8_SB(1, 1), b3 + HSTEP); PG8_STAGE_A(PG8_SA(1, 0), a3, 0);
;             PG8_WAIT_V(8); PG8_WAIT_L(0); PG8_BAR; PG8_MMA(1, 0, At, B0); PG8_MMA(1, 1, At, B1); PG8_BAR; PG8_SCHED;
.LBB0_619:
	s_add_u32 s24, s22, 0x100
	s_addc_u32 s25, s23, 0
	ds_read_b128 v[132:135], v143
	ds_read_b128 v[148:151], v143 offset:1024
	ds_read_b128 v[152:155], v143 offset:2048
	ds_read_b128 v[156:159], v143 offset:3072
	ds_read_b128 v[160:163], v144
	ds_read_b128 v[164:167], v144 offset:1024
	ds_read_b128 v[168:171], v144 offset:2048
	ds_read_b128 v[172:175], v144 offset:3072
	s_cmp_eq_u32 s81, 28
	s_cselect_b32 s34, s52, s24
	s_cselect_b32 s35, s13, s25
	s_cselect_b32 s28, s53, s79
	s_cselect_b32 s29, s11, s80
	s_add_u32 s26, s34, 0x80
	s_addc_u32 s27, s35, 0
	s_add_u32 s22, s22, 0x80
	s_addc_u32 s23, s23, 0
	ds_read_b128 v[176:179], v145
	ds_read_b128 v[180:183], v145 offset:1024
	ds_read_b128 v[184:187], v145 offset:2048
	ds_read_b128 v[188:191], v145 offset:3072
	ds_read_b128 v[192:195], v145 offset:4096
	ds_read_b128 v[196:199], v145 offset:5120
	ds_read_b128 v[200:203], v145 offset:6144
	ds_read_b128 v[204:207], v145 offset:7168
	s_mov_b32 s82, m0
	s_mov_b32 m0, s77
	s_nop 0
	global_load_lds_dwordx4 v141, s[22:23]
	s_mov_b32 m0, s82
	s_nop 0
	s_mov_b32 s82, m0
	s_mov_b32 m0, s78
	s_nop 0
	global_load_lds_dwordx4 v142, s[22:23]
	s_mov_b32 m0, s82
	s_waitcnt vmcnt(8)
	s_waitcnt lgkmcnt(0)
	s_barrier
	s_setprio 1
	v_mfma_f32_16x16x32_bf16 v[126:129], v[132:135], v[176:179], v[126:129]
	v_mfma_f32_16x16x32_bf16 v[122:125], v[152:155], v[176:179], v[122:125]
	v_mfma_f32_16x16x32_bf16 v[118:121], v[132:135], v[184:187], v[118:121]
	v_mfma_f32_16x16x32_bf16 v[114:117], v[152:155], v[184:187], v[114:117]
	v_mfma_f32_16x16x32_bf16 v[94:97], v[132:135], v[192:195], v[94:97]
	v_mfma_f32_16x16x32_bf16 v[90:93], v[152:155], v[192:195], v[90:93]
	v_mfma_f32_16x16x32_bf16 v[86:89], v[132:135], v[200:203], v[86:89]
	v_mfma_f32_16x16x32_bf16 v[74:77], v[152:155], v[200:203], v[74:77]
	v_mfma_f32_16x16x32_bf16 v[126:129], v[148:151], v[180:183], v[126:129]
	v_mfma_f32_16x16x32_bf16 v[122:125], v[156:159], v[180:183], v[122:125]
	v_mfma_f32_16x16x32_bf16 v[118:121], v[148:151], v[188:191], v[118:121]
	v_mfma_f32_16x16x32_bf16 v[114:117], v[156:159], v[188:191], v[114:117]
	v_mfma_f32_16x16x32_bf16 v[94:97], v[148:151], v[196:199], v[94:97]
	v_mfma_f32_16x16x32_bf16 v[90:93], v[156:159], v[196:199], v[90:93]
	v_mfma_f32_16x16x32_bf16 v[86:89], v[148:151], v[204:207], v[86:89]
	v_mfma_f32_16x16x32_bf16 v[74:77], v[156:159], v[204:207], v[74:77]
	s_setprio 0
	s_setprio 1
	v_mfma_f32_16x16x32_bf16 v[110:113], v[160:163], v[176:179], v[110:113]
	s_add_u32 s22, s28, 0x80
	s_addc_u32 s23, s29, 0
	v_mfma_f32_16x16x32_bf16 v[106:109], v[168:171], v[176:179], v[106:109]
	v_mfma_f32_16x16x32_bf16 v[102:105], v[160:163], v[184:187], v[102:105]
	v_mfma_f32_16x16x32_bf16 v[98:101], v[168:171], v[184:187], v[98:101]
	v_mfma_f32_16x16x32_bf16 v[82:85], v[160:163], v[192:195], v[82:85]
	v_mfma_f32_16x16x32_bf16 v[78:81], v[168:171], v[192:195], v[78:81]
	v_mfma_f32_16x16x32_bf16 v[70:73], v[160:163], v[200:203], v[70:73]
	v_mfma_f32_16x16x32_bf16 v[66:69], v[168:171], v[200:203], v[66:69]
	v_mfma_f32_16x16x32_bf16 v[110:113], v[164:167], v[180:183], v[110:113]
	v_mfma_f32_16x16x32_bf16 v[106:109], v[172:175], v[180:183], v[106:109]
	v_mfma_f32_16x16x32_bf16 v[102:105], v[164:167], v[188:191], v[102:105]
	v_mfma_f32_16x16x32_bf16 v[98:101], v[172:175], v[188:191], v[98:101]
	v_mfma_f32_16x16x32_bf16 v[82:85], v[164:167], v[196:199], v[82:85]
	v_mfma_f32_16x16x32_bf16 v[78:81], v[172:175], v[196:199], v[78:81]
	v_mfma_f32_16x16x32_bf16 v[70:73], v[164:167], v[204:207], v[70:73]
	v_mfma_f32_16x16x32_bf16 v[66:69], v[172:175], v[204:207], v[66:69]
	s_setprio 0
	s_barrier
	ds_read_b128 v[176:179], v145 offset:16384
	ds_read_b128 v[180:183], v145 offset:17408
	ds_read_b128 v[184:187], v145 offset:18432
	ds_read_b128 v[188:191], v145 offset:19456
	ds_read_b128 v[192:195], v145 offset:20480
	ds_read_b128 v[196:199], v145 offset:21504
	ds_read_b128 v[200:203], v145 offset:22528
	ds_read_b128 v[204:207], v145 offset:23552
	s_mov_b32 s82, m0
	s_mov_b32 m0, s39
	s_nop 0
	global_load_lds_dwordx4 v139, s[28:29]
	s_mov_b32 m0, s82
	s_nop 0
	s_mov_b32 s82, m0
	s_mov_b32 m0, s54
	s_nop 0
	global_load_lds_dwordx4 v140, s[28:29]
	s_mov_b32 m0, s82
	s_add_u32 s82, s28, 0x80000
	s_addc_u32 s83, s29, 0
	s_mov_b32 s84, m0
	s_mov_b32 m0, s55
	s_nop 0
	global_load_lds_dwordx4 v139, s[82:83]
	s_mov_b32 m0, s84
	s_nop 0
	s_mov_b32 s84, m0
	s_mov_b32 m0, s56
	s_nop 0
	global_load_lds_dwordx4 v140, s[82:83]
	s_mov_b32 m0, s84
	s_mov_b32 s82, m0
	s_mov_b32 m0, s21
	s_nop 0
	global_load_lds_dwordx4 v139, s[34:35]
	s_mov_b32 m0, s82
	s_nop 0
	s_mov_b32 s82, m0
	s_mov_b32 m0, s57
	s_nop 0
	global_load_lds_dwordx4 v140, s[34:35]
	s_mov_b32 m0, s82
	s_waitcnt vmcnt(8)
	s_waitcnt lgkmcnt(0)
	s_barrier
; #define LAS __attribute__((address_space(3)))
;     __device__ __forceinline__ void a_offs_idx(const Unit& u, const unsigned (&nat)[2], unsigned (&v)[4], const LAS int*) const { a_offs(u, nat, v); }
; #define PG8_STAGE_A(bufoff, gbase, h) do { _Pragma("unroll") for (int _i = 0; _i < 2; ++_i) PG8_GLDS(gbase, va[(h) * 2 + _i], ldsb + (bufoff) + ldsw + _i * 8192); } while (0)
; #define PG8_STAGE_B(bufoff, gbase) do { _Pragma("unroll") for (int _i = 0; _i < 2; ++_i) PG8_GLDS(gbase, voffB[_i], ldsb + (bufoff) + ldsw + _i * 8192); } while (0)
; #define PG8_LDA(dst, b, h) do { _Pragma("unroll") for (int m = 0; m < 4; ++m) _Pragma("unroll") for (int k = 0; k < 2; ++k) dst[m][k] = *(const LAS i32x4*)(lds + PG8_SA(b, h) + aoff + m * 2048 + k * 1024); } while (0)
; #define PG8_LDB(dst, b, h) do { _Pragma("unroll") for (int n = 0; n < 2; ++n) _Pragma("unroll") for (int k = 0; k < 2; ++k) dst[n][k] = *(const LAS i32x4*)(lds + PG8_SB(b, h) + boff + n * 2048 + k * 1024); } while (0)
; #define PG8_WAIT_V(n) asm volatile("s_waitcnt vmcnt(" #n ")" ::: "memory")
; #define PG8_WAIT_L(n) asm volatile("s_waitcnt lgkmcnt(" #n ")" ::: "memory")
; template <class Epi, class Sched>
; __device__ __forceinline__ void gemm_phase(LAS unsigned char* lds, const Sched& S, const Epi& E) {
;     ...
;             PG8_LDB(B0, 0, 0); PG8_LDB(B1, 0, 1); PG8_SCHED; PG8_LDA(At, 0, 0); PG8_STAGE_A(PG8_SA(1, 1), a1, 1);
;             PG8_WAIT_V(8); PG8_WAIT_L(0); PG8_BAR; PG8_MMA(0, 0, At, B0); PG8_MMA(0, 1, At, B1); PG8_BAR; PG8_SCHED;
;             if (last && has_next) S.a_offs_idx(nxt, natA, va, (const LAS int*)(lds + IDX_OFF));
;             PG8_LDA(At, 0, 1); PG8_STAGE_B(PG8_SB(0, 0), b2); PG8_STAGE_B(PG8_SB(0, 1), b2 + HSTEP); PG8_STAGE_A(PG8_SA(0, 0), a2, 0);
;             PG8_WAIT_V(8); PG8_WAIT_L(0); PG8_BAR; PG8_MMA(1, 0, At, B0); PG8_MMA(1, 1, At, B1); PG8_BAR; PG8_SCHED;
;             PG8_LDB(B0, 1, 0); PG8_LDB(B1, 1, 1); PG8_SCHED; PG8_LDA(At, 1, 0); PG8_STAGE_A(PG8_SA(0, 1), a2, 1);
;             PG8_WAIT_V(8); PG8_WAIT_L(0); PG8_BAR; PG8_MMA(0, 0, At, B0); PG8_MMA(0, 1, At, B1); PG8_BAR; PG8_SCHED;
;             PG8_LDA(At, 1, 1); PG8_STAGE_B(PG8_SB(1, 0), b3); PG8_STAGE_B(PG8_SB(1, 1), b3 + HSTEP); PG8_STAGE_A(PG8_SA(1, 0), a3, 0);
;             PG8_WAIT_V(8); PG8_WAIT_L(0); PG8_BAR; PG8_MMA(1, 0, At, B0); PG8_MMA(1, 1, At, B1); PG8_BAR; PG8_SCHED;
	s_setprio 1
	v_mfma_f32_16x16x32_bf16 v[62:65], v[132:135], v[176:179], v[62:65]
	v_mfma_f32_16x16x32_bf16 v[58:61], v[152:155], v[176:179], v[58:61]
	v_mfma_f32_16x16x32_bf16 v[54:57], v[132:135], v[184:187], v[54:57]
	v_mfma_f32_16x16x32_bf16 v[42:45], v[152:155], v[184:187], v[42:45]
	v_mfma_f32_16x16x32_bf16 v[38:41], v[132:135], v[192:195], v[38:41]
	v_mfma_f32_16x16x32_bf16 v[26:29], v[152:155], v[192:195], v[26:29]
	v_mfma_f32_16x16x32_bf16 v[22:25], v[132:135], v[200:203], v[22:25]
	v_mfma_f32_16x16x32_bf16 v[10:13], v[152:155], v[200:203], v[10:13]
	v_mfma_f32_16x16x32_bf16 v[62:65], v[148:151], v[180:183], v[62:65]
	v_mfma_f32_16x16x32_bf16 v[58:61], v[156:159], v[180:183], v[58:61]
	v_mfma_f32_16x16x32_bf16 v[54:57], v[148:151], v[188:191], v[54:57]
	v_mfma_f32_16x16x32_bf16 v[42:45], v[156:159], v[188:191], v[42:45]
	v_mfma_f32_16x16x32_bf16 v[38:41], v[148:151], v[196:199], v[38:41]
	v_mfma_f32_16x16x32_bf16 v[26:29], v[156:159], v[196:199], v[26:29]
	v_mfma_f32_16x16x32_bf16 v[22:25], v[148:151], v[204:207], v[22:25]
	v_mfma_f32_16x16x32_bf16 v[10:13], v[156:159], v[204:207], v[10:13]
	s_setprio 0
	s_setprio 1
	v_mfma_f32_16x16x32_bf16 v[50:53], v[160:163], v[176:179], v[50:53]
	v_mfma_f32_16x16x32_bf16 v[46:49], v[168:171], v[176:179], v[46:49]
	v_mfma_f32_16x16x32_bf16 v[34:37], v[160:163], v[184:187], v[34:37]
	v_mfma_f32_16x16x32_bf16 v[30:33], v[168:171], v[184:187], v[30:33]
	v_mfma_f32_16x16x32_bf16 v[18:21], v[160:163], v[192:195], v[18:21]
	v_mfma_f32_16x16x32_bf16 v[14:17], v[168:171], v[192:195], v[14:17]
	v_mfma_f32_16x16x32_bf16 v[6:9], v[160:163], v[200:203], v[6:9]
	v_mfma_f32_16x16x32_bf16 v[2:5], v[168:171], v[200:203], v[2:5]
	v_mfma_f32_16x16x32_bf16 v[50:53], v[164:167], v[180:183], v[50:53]
	v_mfma_f32_16x16x32_bf16 v[46:49], v[172:175], v[180:183], v[46:49]
	v_mfma_f32_16x16x32_bf16 v[34:37], v[164:167], v[188:191], v[34:37]
	v_mfma_f32_16x16x32_bf16 v[30:33], v[172:175], v[188:191], v[30:33]
	v_mfma_f32_16x16x32_bf16 v[18:21], v[164:167], v[196:199], v[18:21]
	v_mfma_f32_16x16x32_bf16 v[14:17], v[172:175], v[196:199], v[14:17]
	v_mfma_f32_16x16x32_bf16 v[6:9], v[164:167], v[204:207], v[6:9]
	v_mfma_f32_16x16x32_bf16 v[2:5], v[172:175], v[204:207], v[2:5]
	s_setprio 0
	s_barrier
	ds_read_b128 v[132:135], v146
	ds_read_b128 v[148:151], v146 offset:1024
	ds_read_b128 v[152:155], v146 offset:2048
	ds_read_b128 v[156:159], v146 offset:3072
	ds_read_b128 v[160:163], v147
	ds_read_b128 v[164:167], v147 offset:1024
	ds_read_b128 v[168:171], v147 offset:2048
	ds_read_b128 v[172:175], v147 offset:3072
	ds_read_b128 v[176:179], v145 offset:32768
	ds_read_b128 v[180:183], v145 offset:33792
	ds_read_b128 v[184:187], v145 offset:34816
	ds_read_b128 v[188:191], v145 offset:35840
	ds_read_b128 v[192:195], v145 offset:36864
	ds_read_b128 v[196:199], v145 offset:37888
	ds_read_b128 v[200:203], v145 offset:38912
	ds_read_b128 v[204:207], v145 offset:39936
	s_mov_b32 s82, m0
	s_mov_b32 m0, s58
	s_nop 0
	global_load_lds_dwordx4 v141, s[34:35]
	s_mov_b32 m0, s82
	s_nop 0
	s_mov_b32 s82, m0
	s_mov_b32 m0, s59
	s_nop 0
	global_load_lds_dwordx4 v142, s[34:35]
	s_mov_b32 m0, s82
	s_waitcnt vmcnt(8)
	s_waitcnt lgkmcnt(0)
	s_barrier
	s_setprio 1
	v_mfma_f32_16x16x32_bf16 v[126:129], v[132:135], v[176:179], v[126:129]
	v_mfma_f32_16x16x32_bf16 v[122:125], v[152:155], v[176:179], v[122:125]
	v_mfma_f32_16x16x32_bf16 v[118:121], v[132:135], v[184:187], v[118:121]
	v_mfma_f32_16x16x32_bf16 v[114:117], v[152:155], v[184:187], v[114:117]
	v_mfma_f32_16x16x32_bf16 v[94:97], v[132:135], v[192:195], v[94:97]
	v_mfma_f32_16x16x32_bf16 v[90:93], v[152:155], v[192:195], v[90:93]
	v_mfma_f32_16x16x32_bf16 v[86:89], v[132:135], v[200:203], v[86:89]
	v_mfma_f32_16x16x32_bf16 v[74:77], v[152:155], v[200:203], v[74:77]
	v_mfma_f32_16x16x32_bf16 v[126:129], v[148:151], v[180:183], v[126:129]
	v_mfma_f32_16x16x32_bf16 v[122:125], v[156:159], v[180:183], v[122:125]
	v_mfma_f32_16x16x32_bf16 v[118:121], v[148:151], v[188:191], v[118:121]
	v_mfma_f32_16x16x32_bf16 v[114:117], v[156:159], v[188:191], v[114:117]
	v_mfma_f32_16x16x32_bf16 v[94:97], v[148:151], v[196:199], v[94:97]
	v_mfma_f32_16x16x32_bf16 v[90:93], v[156:159], v[196:199], v[90:93]
	v_mfma_f32_16x16x32_bf16 v[86:89], v[148:151], v[204:207], v[86:89]
	v_mfma_f32_16x16x32_bf16 v[74:77], v[156:159], v[204:207], v[74:77]
	s_setprio 0
	s_setprio 1
	v_mfma_f32_16x16x32_bf16 v[110:113], v[160:163], v[176:179], v[110:113]
	v_mfma_f32_16x16x32_bf16 v[106:109], v[168:171], v[176:179], v[106:109]
	v_mfma_f32_16x16x32_bf16 v[102:105], v[160:163], v[184:187], v[102:105]
	v_mfma_f32_16x16x32_bf16 v[98:101], v[168:171], v[184:187], v[98:101]
	v_mfma_f32_16x16x32_bf16 v[82:85], v[160:163], v[192:195], v[82:85]
	v_mfma_f32_16x16x32_bf16 v[78:81], v[168:171], v[192:195], v[78:81]
	v_mfma_f32_16x16x32_bf16 v[70:73], v[160:163], v[200:203], v[70:73]
	v_mfma_f32_16x16x32_bf16 v[66:69], v[168:171], v[200:203], v[66:69]
	v_mfma_f32_16x16x32_bf16 v[110:113], v[164:167], v[180:183], v[110:113]
	v_mfma_f32_16x16x32_bf16 v[106:109], v[172:175], v[180:183], v[106:109]
	v_mfma_f32_16x16x32_bf16 v[102:105], v[164:167], v[188:191], v[102:105]
	v_mfma_f32_16x16x32_bf16 v[98:101], v[172:175], v[188:191], v[98:101]
	v_mfma_f32_16x16x32_bf16 v[82:85], v[164:167], v[196:199], v[82:85]
	v_mfma_f32_16x16x32_bf16 v[78:81], v[172:175], v[196:199], v[78:81]
	v_mfma_f32_16x16x32_bf16 v[70:73], v[164:167], v[204:207], v[70:73]
	v_mfma_f32_16x16x32_bf16 v[66:69], v[172:175], v[204:207], v[66:69]
	s_setprio 0
	s_barrier
; #define LAS __attribute__((address_space(3)))
;     __device__ __forceinline__ void a_offs_idx(const Unit& u, const unsigned (&nat)[2], unsigned (&v)[4], const LAS int*) const { a_offs(u, nat, v); }
; #define PG8_STAGE_A(bufoff, gbase, h) do { _Pragma("unroll") for (int _i = 0; _i < 2; ++_i) PG8_GLDS(gbase, va[(h) * 2 + _i], ldsb + (bufoff) + ldsw + _i * 8192); } while (0)
; #define PG8_STAGE_B(bufoff, gbase) do { _Pragma("unroll") for (int _i = 0; _i < 2; ++_i) PG8_GLDS(gbase, voffB[_i], ldsb + (bufoff) + ldsw + _i * 8192); } while (0)
; #define PG8_LDA(dst, b, h) do { _Pragma("unroll") for (int m = 0; m < 4; ++m) _Pragma("unroll") for (int k = 0; k < 2; ++k) dst[m][k] = *(const LAS i32x4*)(lds + PG8_SA(b, h) + aoff + m * 2048 + k * 1024); } while (0)
; #define PG8_LDB(dst, b, h) do { _Pragma("unroll") for (int n = 0; n < 2; ++n) _Pragma("unroll") for (int k = 0; k < 2; ++k) dst[n][k] = *(const LAS i32x4*)(lds + PG8_SB(b, h) + boff + n * 2048 + k * 1024); } while (0)
; #define PG8_WAIT_V(n) asm volatile("s_waitcnt vmcnt(" #n ")" ::: "memory")
; #define PG8_WAIT_L(n) asm volatile("s_waitcnt lgkmcnt(" #n ")" ::: "memory")
; template <class Epi, class Sched>
; __device__ __forceinline__ void gemm_phase(LAS unsigned char* lds, const Sched& S, const Epi& E) {
;     ...
;             PG8_LDB(B0, 0, 0); PG8_LDB(B1, 0, 1); PG8_SCHED; PG8_LDA(At, 0, 0); PG8_STAGE_A(PG8_SA(1, 1), a1, 1);
;             PG8_WAIT_V(8); PG8_WAIT_L(0); PG8_BAR; PG8_MMA(0, 0, At, B0); PG8_MMA(0, 1, At, B1); PG8_BAR; PG8_SCHED;
;             if (last && has_next) S.a_offs_idx(nxt, natA, va, (const LAS int*)(lds + IDX_OFF));
;             PG8_LDA(At, 0, 1); PG8_STAGE_B(PG8_SB(0, 0), b2); PG8_STAGE_B(PG8_SB(0, 1), b2 + HSTEP); PG8_STAGE_A(PG8_SA(0, 0), a2, 0);
;             PG8_WAIT_V(8); PG8_WAIT_L(0); PG8_BAR; PG8_MMA(1, 0, At, B0); PG8_MMA(1, 1, At, B1); PG8_BAR; PG8_SCHED;
;             PG8_LDB(B0, 1, 0); PG8_LDB(B1, 1, 1); PG8_SCHED; PG8_LDA(At, 1, 0); PG8_STAGE_A(PG8_SA(0, 1), a2, 1);
;             PG8_WAIT_V(8); PG8_WAIT_L(0); PG8_BAR; PG8_MMA(0, 0, At, B0); PG8_MMA(0, 1, At, B1); PG8_BAR; PG8_SCHED;
;             PG8_LDA(At, 1, 1); PG8_STAGE_B(PG8_SB(1, 0), b3); PG8_STAGE_B(PG8_SB(1, 1), b3 + HSTEP); PG8_STAGE_A(PG8_SA(1, 0), a3, 0);
;             PG8_WAIT_V(8); PG8_WAIT_L(0); PG8_BAR; PG8_MMA(1, 0, At, B0); PG8_MMA(1, 1, At, B1); PG8_BAR; PG8_SCHED;
	ds_read_b128 v[176:179], v145 offset:49152
	ds_read_b128 v[180:183], v145 offset:50176
	ds_read_b128 v[184:187], v145 offset:51200
	ds_read_b128 v[188:191], v145 offset:52224
	ds_read_b128 v[192:195], v145 offset:53248
	ds_read_b128 v[196:199], v145 offset:54272
	ds_read_b128 v[200:203], v145 offset:55296
	ds_read_b128 v[204:207], v145 offset:56320
	s_mov_b32 s34, m0
	s_mov_b32 m0, s63
	s_nop 0
	global_load_lds_dwordx4 v139, s[22:23]
	s_mov_b32 m0, s34
	s_nop 0
	s_mov_b32 s34, m0
	s_mov_b32 m0, s64
	s_nop 0
	global_load_lds_dwordx4 v140, s[22:23]
	s_mov_b32 m0, s34
	s_add_u32 s22, s28, 0x80080
	s_addc_u32 s23, s29, 0
	s_mov_b32 s28, m0
	s_mov_b32 m0, s67
	s_nop 0
	global_load_lds_dwordx4 v139, s[22:23]
	s_mov_b32 m0, s28
	s_nop 0
	s_mov_b32 s28, m0
	s_mov_b32 m0, s76
	s_nop 0
	global_load_lds_dwordx4 v140, s[22:23]
	s_mov_b32 m0, s28
	s_mov_b32 s22, m0
	s_mov_b32 m0, s65
	s_nop 0
	global_load_lds_dwordx4 v139, s[26:27]
	s_mov_b32 m0, s22
	s_nop 0
	s_mov_b32 s22, m0
	s_mov_b32 m0, s66
	s_nop 0
	global_load_lds_dwordx4 v140, s[26:27]
	s_mov_b32 m0, s22
	s_waitcnt vmcnt(8)
	s_waitcnt lgkmcnt(0)
	s_barrier
	s_setprio 1
	v_mfma_f32_16x16x32_bf16 v[62:65], v[132:135], v[176:179], v[62:65]
	v_mfma_f32_16x16x32_bf16 v[58:61], v[152:155], v[176:179], v[58:61]
	v_mfma_f32_16x16x32_bf16 v[54:57], v[132:135], v[184:187], v[54:57]
	v_mfma_f32_16x16x32_bf16 v[42:45], v[152:155], v[184:187], v[42:45]
	v_mfma_f32_16x16x32_bf16 v[38:41], v[132:135], v[192:195], v[38:41]
	v_mfma_f32_16x16x32_bf16 v[26:29], v[152:155], v[192:195], v[26:29]
	v_mfma_f32_16x16x32_bf16 v[22:25], v[132:135], v[200:203], v[22:25]
	v_mfma_f32_16x16x32_bf16 v[10:13], v[152:155], v[200:203], v[10:13]
	v_mfma_f32_16x16x32_bf16 v[62:65], v[148:151], v[180:183], v[62:65]
	v_mfma_f32_16x16x32_bf16 v[58:61], v[156:159], v[180:183], v[58:61]
	v_mfma_f32_16x16x32_bf16 v[54:57], v[148:151], v[188:191], v[54:57]
	v_mfma_f32_16x16x32_bf16 v[42:45], v[156:159], v[188:191], v[42:45]
	v_mfma_f32_16x16x32_bf16 v[38:41], v[148:151], v[196:199], v[38:41]
	v_mfma_f32_16x16x32_bf16 v[26:29], v[156:159], v[196:199], v[26:29]
	v_mfma_f32_16x16x32_bf16 v[22:25], v[148:151], v[204:207], v[22:25]
	v_mfma_f32_16x16x32_bf16 v[10:13], v[156:159], v[204:207], v[10:13]
	s_setprio 0
	s_setprio 1
	v_mfma_f32_16x16x32_bf16 v[50:53], v[160:163], v[176:179], v[50:53]
	v_mfma_f32_16x16x32_bf16 v[46:49], v[168:171], v[176:179], v[46:49]
	v_mfma_f32_16x16x32_bf16 v[34:37], v[160:163], v[184:187], v[34:37]
	v_mfma_f32_16x16x32_bf16 v[30:33], v[168:171], v[184:187], v[30:33]
	v_mfma_f32_16x16x32_bf16 v[18:21], v[160:163], v[192:195], v[18:21]
	v_mfma_f32_16x16x32_bf16 v[14:17], v[168:171], v[192:195], v[14:17]
	v_mfma_f32_16x16x32_bf16 v[6:9], v[160:163], v[200:203], v[6:9]
	v_mfma_f32_16x16x32_bf16 v[2:5], v[168:171], v[200:203], v[2:5]
	v_mfma_f32_16x16x32_bf16 v[50:53], v[164:167], v[180:183], v[50:53]
	v_mfma_f32_16x16x32_bf16 v[46:49], v[172:175], v[180:183], v[46:49]
	v_mfma_f32_16x16x32_bf16 v[34:37], v[164:167], v[188:191], v[34:37]
	v_mfma_f32_16x16x32_bf16 v[30:33], v[172:175], v[188:191], v[30:33]
	v_mfma_f32_16x16x32_bf16 v[18:21], v[164:167], v[196:199], v[18:21]
	v_mfma_f32_16x16x32_bf16 v[14:17], v[172:175], v[196:199], v[14:17]
	v_mfma_f32_16x16x32_bf16 v[6:9], v[164:167], v[204:207], v[6:9]
	v_mfma_f32_16x16x32_bf16 v[2:5], v[172:175], v[204:207], v[2:5]
	s_setprio 0
	s_barrier
	s_add_i32 s81, s81, 2
	s_add_u32 s79, s79, 0x100
	s_addc_u32 s80, s80, 0
	s_cmp_gt_u32 s81, 29
	s_mov_b64 s[22:23], s[24:25]
	s_cbranch_scc0 .LBB0_619
	s_mov_b32 s13, s95
	s_and_b64 vcc, exec, s[8:9]
	s_cbranch_vccz .LBB0_622
	s_barrier

; #define LAS __attribute__((address_space(3)))
;     __device__ __forceinline__ void a_offs_idx(const Unit& u, const unsigned (&nat)[2], unsigned (&v)[4], const LAS int*) const { a_offs(u, nat, v); }
; #define PG8_STAGE_A(bufoff, gbase, h) do { _Pragma("unroll") for (int _i = 0; _i < 2; ++_i) PG8_GLDS(gbase, va[(h) * 2 + _i], ldsb + (bufoff) + ldsw + _i * 8192); } while (0)
; #define PG8_STAGE_B(bufoff, gbase) do { _Pragma("unroll") for (int _i = 0; _i < 2; ++_i) PG8_GLDS(gbase, voffB[_i], ldsb + (bufoff) + ldsw + _i * 8192); } while (0)
; #define PG8_LDA(dst, b, h) do { _Pragma("unroll") for (int m = 0; m < 4; ++m) _Pragma("unroll") for (int k = 0; k < 2; ++k) dst[m][k] = *(const LAS i32x4*)(lds + PG8_SA(b, h) + aoff + m * 2048 + k * 1024); } while (0)
; #define PG8_LDB(dst, b, h) do { _Pragma("unroll") for (int n = 0; n < 2; ++n) _Pragma("unroll") for (int k = 0; k < 2; ++k) dst[n][k] = *(const LAS i32x4*)(lds + PG8_SB(b, h) + boff + n * 2048 + k * 1024); } while (0)
; #define PG8_WAIT_V(n) asm volatile("s_waitcnt vmcnt(" #n ")" ::: "memory")
; #define PG8_WAIT_L(n) asm volatile("s_waitcnt lgkmcnt(" #n ")" ::: "memory")
; template <class Epi, class Sched>
; __device__ __forceinline__ void gemm_phase(LAS unsigned char* lds, const Sched& S, const Epi& E) {
;     ...
;             PG8_LDB(B0, 0, 0); PG8_LDB(B1, 0, 1); PG8_SCHED; PG8_LDA(At, 0, 0); PG8_STAGE_A(PG8_SA(1, 1), a1, 1);
;             PG8_WAIT_V(8); PG8_WAIT_L(0); PG8_BAR; PG8_MMA(0, 0, At, B0); PG8_MMA(0, 1, At, B1); PG8_BAR; PG8_SCHED;
;             if (last && has_next) S.a_offs_idx(nxt, natA, va, (const LAS int*)(lds + IDX_OFF));
;             PG8_LDA(At, 0, 1); PG8_STAGE_B(PG8_SB(0, 0), b2); PG8_STAGE_B(PG8_SB(0, 1), b2 + HSTEP); PG8_STAGE_A(PG8_SA(0, 0), a2, 0);
;             PG8_WAIT_V(8); PG8_WAIT_L(0); PG8_BAR; PG8_MMA(1, 0, At, B0); PG8_MMA(1, 1, At, B1); PG8_BAR; PG8_SCHED;
;             PG8_LDB(B0, 1, 0); PG8_LDB(B1, 1, 1); PG8_SCHED; PG8_LDA(At, 1, 0); PG8_STAGE_A(PG8_SA(0, 1), a2, 1);
;             PG8_WAIT_V(8); PG8_WAIT_L(0); PG8_BAR; PG8_MMA(0, 0, At, B0); PG8_MMA(0, 1, At, B1); PG8_BAR; PG8_SCHED;
;             PG8_LDA(At, 1, 1); PG8_STAGE_B(PG8_SB(1, 0), b3); PG8_STAGE_B(PG8_SB(1, 1), b3 + HSTEP); PG8_STAGE_A(PG8_SA(1, 0), a3, 0);
;             PG8_WAIT_V(8); PG8_WAIT_L(0); PG8_BAR; PG8_MMA(1, 0, At, B0); PG8_MMA(1, 1, At, B1); PG8_BAR; PG8_SCHED;
.LBB0_1010:
	s_add_u32 s58, s58, 0x100
	s_addc_u32 s59, s59, 0
	s_and_b64 s[62:63], s[60:61], exec
	s_cselect_b32 s66, s18, s58
	s_cselect_b32 s67, s19, s59
	s_add_u32 s62, s66, 0x80
	s_addc_u32 s63, s67, 0
	s_and_b64 s[60:61], s[60:61], exec
	s_cselect_b32 s60, s44, s41
	s_cselect_b32 s61, s45, s43
	s_add_u32 s64, s60, 0x80
	s_addc_u32 s65, s61, 0
	ds_read_b128 v[130:133], v214 offset:16384
	ds_read_b128 v[134:137], v214 offset:17408
	ds_read_b128 v[146:149], v214 offset:18432
	ds_read_b128 v[150:153], v214 offset:19456
	ds_read_b128 v[162:165], v214 offset:20480
	ds_read_b128 v[166:169], v214 offset:21504
	ds_read_b128 v[216:219], v214 offset:22528
	ds_read_b128 v[220:223], v214 offset:23552
	s_mov_b32 s12, m0
	s_mov_b32 m0, s30
	s_nop 0
	global_load_lds_dwordx4 v194, s[60:61]
	s_mov_b32 m0, s12
	s_nop 0
	s_mov_b32 s12, m0
	s_mov_b32 m0, s31
	s_nop 0
	global_load_lds_dwordx4 v201, s[60:61]
	s_mov_b32 m0, s12
	s_add_u32 s12, s60, 0x40000
	s_addc_u32 s13, s61, 0
	s_mov_b32 vcc_lo, m0
	s_mov_b32 m0, s36
	s_nop 0
	global_load_lds_dwordx4 v194, s[12:13]
	s_mov_b32 m0, vcc_lo
	s_nop 0
	s_mov_b32 vcc_lo, m0
	s_mov_b32 m0, s55
	s_nop 0
	global_load_lds_dwordx4 v201, s[12:13]
	s_mov_b32 m0, vcc_lo
	s_mov_b32 s12, m0
	s_mov_b32 m0, s29
	s_nop 0
	global_load_lds_dwordx4 v204, s[66:67]
	s_mov_b32 m0, s12
	s_nop 0
	s_mov_b32 s12, m0
	s_mov_b32 m0, s85
	s_nop 0
	global_load_lds_dwordx4 v205, s[66:67]
	s_mov_b32 m0, s12
	s_waitcnt vmcnt(8)
	s_waitcnt lgkmcnt(0)
	s_barrier
	s_setprio 1
	v_mfma_scale_f32_16x16x128_f8f6f4 v[126:129], v[18:25], v[130:137], v[126:129], v199, v199 op_sel_hi:[0,0,0]
	v_mfma_scale_f32_16x16x128_f8f6f4 v[122:125], v[26:33], v[130:137], v[122:125], v199, v199 op_sel_hi:[0,0,0]
	v_mfma_scale_f32_16x16x128_f8f6f4 v[110:113], v[18:25], v[146:153], v[110:113], v199, v199 op_sel_hi:[0,0,0]
	v_mfma_scale_f32_16x16x128_f8f6f4 v[106:109], v[26:33], v[146:153], v[106:109], v199, v199 op_sel_hi:[0,0,0]
	v_mfma_scale_f32_16x16x128_f8f6f4 v[224:227], v[18:25], v[162:169], v[94:97], v199, v199 op_sel_hi:[0,0,0]
	v_mfma_scale_f32_16x16x128_f8f6f4 v[228:231], v[26:33], v[162:169], v[90:93], v199, v199 op_sel_hi:[0,0,0]
	v_mfma_scale_f32_16x16x128_f8f6f4 v[232:235], v[18:25], v[216:223], v[78:81], v199, v199 op_sel_hi:[0,0,0]
	v_mfma_scale_f32_16x16x128_f8f6f4 v[236:239], v[26:33], v[216:223], v[74:77], v199, v199 op_sel_hi:[0,0,0]
	s_setprio 0
	s_setprio 1
	v_mfma_scale_f32_16x16x128_f8f6f4 v[118:121], v[2:9], v[130:137], v[118:121], v199, v199 op_sel_hi:[0,0,0]
	v_mfma_scale_f32_16x16x128_f8f6f4 v[114:117], v[10:17], v[130:137], v[114:117], v199, v199 op_sel_hi:[0,0,0]
	v_mfma_scale_f32_16x16x128_f8f6f4 v[102:105], v[2:9], v[146:153], v[102:105], v199, v199 op_sel_hi:[0,0,0]
	v_mfma_scale_f32_16x16x128_f8f6f4 v[98:101], v[10:17], v[146:153], v[98:101], v199, v199 op_sel_hi:[0,0,0]
	v_mfma_scale_f32_16x16x128_f8f6f4 v[240:243], v[2:9], v[162:169], v[86:89], v199, v199 op_sel_hi:[0,0,0]
	v_mfma_scale_f32_16x16x128_f8f6f4 v[244:247], v[10:17], v[162:169], v[82:85], v199, v199 op_sel_hi:[0,0,0]
	v_mfma_scale_f32_16x16x128_f8f6f4 v[248:251], v[2:9], v[216:223], v[70:73], v199, v199 op_sel_hi:[0,0,0]
	v_mfma_scale_f32_16x16x128_f8f6f4 v[216:219], v[10:17], v[216:223], v[66:69], v199, v199 op_sel_hi:[0,0,0]
	s_setprio 0
	s_barrier
	v_add_u32_e32 v14, 0x18000, v213
	v_add_u32_e32 v30, 0x1c000, v213
	ds_read_b128 v[2:5], v14
	ds_read_b128 v[6:9], v14 offset:1024
	ds_read_b128 v[10:13], v14 offset:2048
	ds_read_b128 v[14:17], v14 offset:3072
	ds_read_b128 v[18:21], v30
	ds_read_b128 v[22:25], v30 offset:1024
	ds_read_b128 v[26:29], v30 offset:2048
	ds_read_b128 v[30:33], v30 offset:3072
	ds_read_b128 v[66:69], v214 offset:32768
	ds_read_b128 v[70:73], v214 offset:33792
	ds_read_b128 v[74:77], v214 offset:34816
	ds_read_b128 v[78:81], v214 offset:35840
	ds_read_b128 v[82:85], v214 offset:36864
	ds_read_b128 v[86:89], v214 offset:37888
	ds_read_b128 v[90:93], v214 offset:38912
	ds_read_b128 v[94:97], v214 offset:39936
	s_mov_b32 s12, m0
	s_mov_b32 m0, s16
	s_nop 0
	global_load_lds_dwordx4 v206, s[66:67]
	s_mov_b32 m0, s12
	s_nop 0
	s_mov_b32 s12, m0
	s_mov_b32 m0, s17
	s_nop 0
	global_load_lds_dwordx4 v207, s[66:67]
	s_mov_b32 m0, s12
	s_waitcnt vmcnt(8)
	s_waitcnt lgkmcnt(0)
	s_barrier
; #define PG8_STAGE_A(bufoff, gbase, h) do { _Pragma("unroll") for (int _i = 0; _i < 2; ++_i) PG8_GLDS(gbase, va[(h) * 2 + _i], ldsb + (bufoff) + ldsw + _i * 8192); } while (0)
; #define PG8_STAGE_B(bufoff, gbase) do { _Pragma("unroll") for (int _i = 0; _i < 2; ++_i) PG8_GLDS(gbase, voffB[_i], ldsb + (bufoff) + ldsw + _i * 8192); } while (0)
; #define PG8_LDA(dst, b, h) do { _Pragma("unroll") for (int m = 0; m < 4; ++m) _Pragma("unroll") for (int k = 0; k < 2; ++k) dst[m][k] = *(const LAS i32x4*)(lds + PG8_SA(b, h) + aoff + m * 2048 + k * 1024); } while (0)
; #define PG8_LDB(dst, b, h) do { _Pragma("unroll") for (int n = 0; n < 2; ++n) _Pragma("unroll") for (int k = 0; k < 2; ++k) dst[n][k] = *(const LAS i32x4*)(lds + PG8_SB(b, h) + boff + n * 2048 + k * 1024); } while (0)
; #define PG8_WAIT_V(n) asm volatile("s_waitcnt vmcnt(" #n ")" ::: "memory")
; #define PG8_WAIT_L(n) asm volatile("s_waitcnt lgkmcnt(" #n ")" ::: "memory")
; #define PG8_BAR __builtin_amdgcn_s_barrier()
; #define PG8_SCHED __builtin_amdgcn_sched_barrier(0)
; template <class Epi, class Sched>
; __device__ __forceinline__ void gemm_phase(LAS unsigned char* lds, const Sched& S, const Epi& E) {
;     ...
;             PG8_WAIT_V(8); PG8_WAIT_L(0); PG8_BAR; PG8_MMA(1, 0, At, B0); PG8_MMA(1, 1, At, B1); PG8_BAR; PG8_SCHED;
;             PG8_LDB(B0, 1, 0); PG8_LDB(B1, 1, 1); PG8_SCHED; PG8_LDA(At, 1, 0); PG8_STAGE_A(PG8_SA(0, 1), a2, 1);
;             PG8_WAIT_V(8); PG8_WAIT_L(0); PG8_BAR; PG8_MMA(0, 0, At, B0); PG8_MMA(0, 1, At, B1); PG8_BAR; PG8_SCHED;
;             PG8_LDA(At, 1, 1); PG8_STAGE_B(PG8_SB(1, 0), b3); PG8_STAGE_B(PG8_SB(1, 1), b3 + HSTEP); PG8_STAGE_A(PG8_SA(1, 0), a3, 0);
;             PG8_WAIT_V(8); PG8_WAIT_L(0); PG8_BAR; PG8_MMA(1, 0, At, B0); PG8_MMA(1, 1, At, B1); PG8_BAR; PG8_SCHED;
;         }
	s_setprio 1
	v_mfma_scale_f32_16x16x128_f8f6f4 v[190:193], v[2:9], v[66:73], v[190:193], v199, v199 op_sel_hi:[0,0,0]
	v_mfma_scale_f32_16x16x128_f8f6f4 v[186:189], v[10:17], v[66:73], v[186:189], v199, v199 op_sel_hi:[0,0,0]
	v_mfma_scale_f32_16x16x128_f8f6f4 v[174:177], v[2:9], v[74:81], v[174:177], v199, v199 op_sel_hi:[0,0,0]
	v_mfma_scale_f32_16x16x128_f8f6f4 v[170:173], v[10:17], v[74:81], v[170:173], v199, v199 op_sel_hi:[0,0,0]
	v_mfma_scale_f32_16x16x128_f8f6f4 v[158:161], v[2:9], v[82:89], v[158:161], v199, v199 op_sel_hi:[0,0,0]
	v_mfma_scale_f32_16x16x128_f8f6f4 v[154:157], v[10:17], v[82:89], v[154:157], v199, v199 op_sel_hi:[0,0,0]
	v_mfma_scale_f32_16x16x128_f8f6f4 v[142:145], v[2:9], v[90:97], v[142:145], v199, v199 op_sel_hi:[0,0,0]
	v_mfma_scale_f32_16x16x128_f8f6f4 v[138:141], v[10:17], v[90:97], v[138:141], v199, v199 op_sel_hi:[0,0,0]
	s_setprio 0
	s_setprio 1
	v_mfma_scale_f32_16x16x128_f8f6f4 v[182:185], v[18:25], v[66:73], v[182:185], v199, v199 op_sel_hi:[0,0,0]
	v_mfma_scale_f32_16x16x128_f8f6f4 v[178:181], v[26:33], v[66:73], v[58:61], v199, v199 op_sel_hi:[0,0,0]
	v_mfma_scale_f32_16x16x128_f8f6f4 v[166:169], v[18:25], v[74:81], v[62:65], v199, v199 op_sel_hi:[0,0,0]
	v_mfma_scale_f32_16x16x128_f8f6f4 v[162:165], v[26:33], v[74:81], v[50:53], v199, v199 op_sel_hi:[0,0,0]
	v_mfma_scale_f32_16x16x128_f8f6f4 v[150:153], v[18:25], v[82:89], v[54:57], v199, v199 op_sel_hi:[0,0,0]
	v_mfma_scale_f32_16x16x128_f8f6f4 v[146:149], v[26:33], v[82:89], v[42:45], v199, v199 op_sel_hi:[0,0,0]
	v_mfma_scale_f32_16x16x128_f8f6f4 v[134:137], v[18:25], v[90:97], v[46:49], v199, v199 op_sel_hi:[0,0,0]
	v_mfma_scale_f32_16x16x128_f8f6f4 v[130:133], v[26:33], v[90:97], v[34:37], v199, v199 op_sel_hi:[0,0,0]
	s_setprio 0
	s_barrier
	s_nop 4
	ds_read_b128 v[34:37], v214 offset:49152
	ds_read_b128 v[38:41], v214 offset:50176
	ds_read_b128 v[42:45], v214 offset:51200
	ds_read_b128 v[46:49], v214 offset:52224
	ds_read_b128 v[50:53], v214 offset:53248
	ds_read_b128 v[54:57], v214 offset:54272
	ds_read_b128 v[58:61], v214 offset:55296
	ds_read_b128 v[62:65], v214 offset:56320
	s_mov_b32 s12, m0
	s_mov_b32 m0, s14
	s_nop 0
	global_load_lds_dwordx4 v194, s[64:65]
	s_mov_b32 m0, s12
	s_nop 0
	s_mov_b32 s12, m0
	s_mov_b32 m0, s26
	s_nop 0
	global_load_lds_dwordx4 v201, s[64:65]
	s_mov_b32 m0, s12
	s_add_u32 s12, s60, 0x40080
	s_addc_u32 s13, s61, 0
	s_mov_b32 s60, m0
	s_mov_b32 m0, s95
	s_nop 0
	global_load_lds_dwordx4 v194, s[12:13]
	s_mov_b32 m0, s60
	s_nop 0
	s_mov_b32 s60, m0
	s_mov_b32 m0, s92
	s_nop 0
	global_load_lds_dwordx4 v201, s[12:13]
	s_mov_b32 m0, s60
	s_mov_b32 s12, m0
	s_mov_b32 m0, s27
	s_nop 0
	global_load_lds_dwordx4 v204, s[62:63]
	s_mov_b32 m0, s12
	s_nop 0
	s_mov_b32 s12, m0
	s_mov_b32 m0, s28
	s_nop 0
	global_load_lds_dwordx4 v205, s[62:63]
	s_mov_b32 m0, s12
	s_waitcnt vmcnt(8)
	s_waitcnt lgkmcnt(0)
	s_barrier
	s_setprio 1
	v_mfma_scale_f32_16x16x128_f8f6f4 v[126:129], v[2:9], v[34:41], v[126:129], v199, v199 op_sel_hi:[0,0,0]
	v_mfma_scale_f32_16x16x128_f8f6f4 v[122:125], v[10:17], v[34:41], v[122:125], v199, v199 op_sel_hi:[0,0,0]
	v_mfma_scale_f32_16x16x128_f8f6f4 v[110:113], v[2:9], v[42:49], v[110:113], v199, v199 op_sel_hi:[0,0,0]
	v_mfma_scale_f32_16x16x128_f8f6f4 v[106:109], v[10:17], v[42:49], v[106:109], v199, v199 op_sel_hi:[0,0,0]
	v_mfma_scale_f32_16x16x128_f8f6f4 v[94:97], v[2:9], v[50:57], v[224:227], v199, v199 op_sel_hi:[0,0,0]
	v_mfma_scale_f32_16x16x128_f8f6f4 v[90:93], v[10:17], v[50:57], v[228:231], v199, v199 op_sel_hi:[0,0,0]
	v_mfma_scale_f32_16x16x128_f8f6f4 v[78:81], v[2:9], v[58:65], v[232:235], v199, v199 op_sel_hi:[0,0,0]
	v_mfma_scale_f32_16x16x128_f8f6f4 v[74:77], v[10:17], v[58:65], v[236:239], v199, v199 op_sel_hi:[0,0,0]
	s_setprio 0
	s_setprio 1
	v_mfma_scale_f32_16x16x128_f8f6f4 v[118:121], v[18:25], v[34:41], v[118:121], v199, v199 op_sel_hi:[0,0,0]
	v_mfma_scale_f32_16x16x128_f8f6f4 v[114:117], v[26:33], v[34:41], v[114:117], v199, v199 op_sel_hi:[0,0,0]
	v_mfma_scale_f32_16x16x128_f8f6f4 v[102:105], v[18:25], v[42:49], v[102:105], v199, v199 op_sel_hi:[0,0,0]
	v_mfma_scale_f32_16x16x128_f8f6f4 v[98:101], v[26:33], v[42:49], v[98:101], v199, v199 op_sel_hi:[0,0,0]
	v_mfma_scale_f32_16x16x128_f8f6f4 v[86:89], v[18:25], v[50:57], v[240:243], v199, v199 op_sel_hi:[0,0,0]
	v_mfma_scale_f32_16x16x128_f8f6f4 v[82:85], v[26:33], v[50:57], v[244:247], v199, v199 op_sel_hi:[0,0,0]
	v_mfma_scale_f32_16x16x128_f8f6f4 v[70:73], v[18:25], v[58:65], v[248:251], v199, v199 op_sel_hi:[0,0,0]
	v_mfma_scale_f32_16x16x128_f8f6f4 v[66:69], v[26:33], v[58:65], v[216:219], v199, v199 op_sel_hi:[0,0,0]
	s_setprio 0
	s_barrier
	s_add_i32 s53, s53, 2
	s_add_u32 s41, s41, 0x100
	s_addc_u32 s43, s43, 0
	s_cmp_gt_u32 s53, 13
	s_cbranch_scc1 .LBB0_1013

; #define LAS __attribute__((address_space(3)))
;     __device__ __forceinline__ void a_offs_idx(const Unit& u, const unsigned (&nat)[2], unsigned (&v)[4], const LAS int*) const { a_offs(u, nat, v); }
; #define PG8_STAGE_A(bufoff, gbase, h) do { _Pragma("unroll") for (int _i = 0; _i < 2; ++_i) PG8_GLDS(gbase, va[(h) * 2 + _i], ldsb + (bufoff) + ldsw + _i * 8192); } while (0)
; #define PG8_STAGE_B(bufoff, gbase) do { _Pragma("unroll") for (int _i = 0; _i < 2; ++_i) PG8_GLDS(gbase, voffB[_i], ldsb + (bufoff) + ldsw + _i * 8192); } while (0)
; #define PG8_LDA(dst, b, h) do { _Pragma("unroll") for (int m = 0; m < 4; ++m) _Pragma("unroll") for (int k = 0; k < 2; ++k) dst[m][k] = *(const LAS i32x4*)(lds + PG8_SA(b, h) + aoff + m * 2048 + k * 1024); } while (0)
; #define PG8_LDB(dst, b, h) do { _Pragma("unroll") for (int n = 0; n < 2; ++n) _Pragma("unroll") for (int k = 0; k < 2; ++k) dst[n][k] = *(const LAS i32x4*)(lds + PG8_SB(b, h) + boff + n * 2048 + k * 1024); } while (0)
; #define PG8_WAIT_V(n) asm volatile("s_waitcnt vmcnt(" #n ")" ::: "memory")
; #define PG8_WAIT_L(n) asm volatile("s_waitcnt lgkmcnt(" #n ")" ::: "memory")
; #define PG8_BAR __builtin_amdgcn_s_barrier()
; #define PG8_SCHED __builtin_amdgcn_sched_barrier(0)
; template <class Epi, class Sched>
; __device__ __forceinline__ void gemm_phase(LAS unsigned char* lds, const Sched& S, const Epi& E) {
;     ...
;         for (int t = 0; t < NTK; t += 2) {
;             const bool last = (t == NTK - 2);
;             const char* a1 = cA + (size_t)(t + 1) * kstep;
;             const char* a2 = last ? nA : cA + (size_t)(t + 2) * kstep; const char* b2 = last ? nB : cB + (size_t)(t + 2) * kstep;
;             const char* a3 = a2 + kstep; const char* b3 = b2 + kstep;
;             PG8_LDB(B0, 0, 0); PG8_LDB(B1, 0, 1); PG8_SCHED; PG8_LDA(At, 0, 0); PG8_STAGE_A(PG8_SA(1, 1), a1, 1);
;             PG8_WAIT_V(8); PG8_WAIT_L(0); PG8_BAR; PG8_MMA(0, 0, At, B0); PG8_MMA(0, 1, At, B1); PG8_BAR; PG8_SCHED;
;             if (last && has_next) S.a_offs_idx(nxt, natA, va, (const LAS int*)(lds + IDX_OFF));
;             PG8_LDA(At, 0, 1); PG8_STAGE_B(PG8_SB(0, 0), b2); PG8_STAGE_B(PG8_SB(0, 1), b2 + HSTEP); PG8_STAGE_A(PG8_SA(0, 0), a2, 0);
;             PG8_WAIT_V(8); PG8_WAIT_L(0); PG8_BAR; PG8_MMA(1, 0, At, B0); PG8_MMA(1, 1, At, B1); PG8_BAR; PG8_SCHED;
.LBB0_1464:
	v_add_u32_e32 v122, 0x10000, v153
	s_add_u32 s48, s44, 0x100
	ds_read_b128 v[156:159], v122
	ds_read_b128 v[160:163], v122 offset:1024
	ds_read_b128 v[164:167], v122 offset:2048
	ds_read_b128 v[168:171], v122 offset:3072
	v_add_u32_e32 v122, 0x14000, v153
	s_addc_u32 s49, s45, 0
	ds_read_b128 v[172:175], v122
	ds_read_b128 v[176:179], v122 offset:1024
	ds_read_b128 v[180:183], v122 offset:2048
	ds_read_b128 v[184:187], v122 offset:3072
	s_cmp_eq_u32 s35, 12
	s_cselect_b32 s56, s36, s48
	s_cselect_b32 s57, s37, s49
	s_cselect_b32 s54, s38, s27
	s_cselect_b32 s55, s39, s29
	s_add_u32 s52, s56, 0x80
	s_addc_u32 s53, s57, 0
	s_add_u32 s44, s44, 0x80
	s_addc_u32 s45, s45, 0
	ds_read_b128 v[188:191], v154
	ds_read_b128 v[192:195], v154 offset:1024
	ds_read_b128 v[196:199], v154 offset:2048
	ds_read_b128 v[200:203], v154 offset:3072
	ds_read_b128 v[204:207], v154 offset:4096
	ds_read_b128 v[208:211], v154 offset:5120
	ds_read_b128 v[212:215], v154 offset:6144
	ds_read_b128 v[216:219], v154 offset:7168
	s_mov_b32 s41, m0
	s_mov_b32 m0, s67
	s_nop 0
	global_load_lds_dwordx4 v151, s[44:45]
	s_mov_b32 m0, s41
	s_nop 0
	s_mov_b32 s41, m0
	s_mov_b32 m0, s61
	s_nop 0
	global_load_lds_dwordx4 v152, s[44:45]
	s_mov_b32 m0, s41
	s_waitcnt vmcnt(8)
	s_waitcnt lgkmcnt(0)
	s_barrier
	s_setprio 1
	v_mfma_scale_f32_16x16x128_f8f6f4 v[126:129], v[164:171], v[188:195], v[126:129], v147, v147 op_sel_hi:[0,0,0]
	v_mfma_scale_f32_16x16x128_f8f6f4 v[118:121], v[156:163], v[196:203], v[118:121], v147, v147 op_sel_hi:[0,0,0]
	v_mfma_scale_f32_16x16x128_f8f6f4 v[114:117], v[164:171], v[196:203], v[114:117], v147, v147 op_sel_hi:[0,0,0]
	v_mfma_scale_f32_16x16x128_f8f6f4 v[110:113], v[156:163], v[204:211], v[110:113], v147, v147 op_sel_hi:[0,0,0]
	v_mfma_scale_f32_16x16x128_f8f6f4 v[106:109], v[164:171], v[204:211], v[106:109], v147, v147 op_sel_hi:[0,0,0]
	v_mfma_scale_f32_16x16x128_f8f6f4 v[102:105], v[156:163], v[212:219], v[102:105], v147, v147 op_sel_hi:[0,0,0]
	v_mfma_scale_f32_16x16x128_f8f6f4 v[98:101], v[164:171], v[212:219], v[98:101], v147, v147 op_sel_hi:[0,0,0]
	v_mfma_scale_f32_16x16x128_f8f6f4 v[122:125], v[156:163], v[188:195], v[130:133], v147, v147 op_sel_hi:[0,0,0]
	s_setprio 0
	s_setprio 1
	s_add_u32 s44, s54, 0x80
	s_addc_u32 s45, s55, 0
	v_mfma_scale_f32_16x16x128_f8f6f4 v[134:137], v[172:179], v[188:195], v[62:65], v147, v147 op_sel_hi:[0,0,0]
	v_mfma_scale_f32_16x16x128_f8f6f4 v[142:145], v[180:187], v[188:195], v[58:61], v147, v147 op_sel_hi:[0,0,0]
	v_mfma_scale_f32_16x16x128_f8f6f4 v[188:191], v[172:179], v[196:203], v[54:57], v147, v147 op_sel_hi:[0,0,0]
	v_mfma_scale_f32_16x16x128_f8f6f4 v[192:195], v[180:187], v[196:203], v[50:53], v147, v147 op_sel_hi:[0,0,0]
	v_mfma_scale_f32_16x16x128_f8f6f4 v[196:199], v[172:179], v[204:211], v[46:49], v147, v147 op_sel_hi:[0,0,0]
	v_mfma_scale_f32_16x16x128_f8f6f4 v[200:203], v[180:187], v[204:211], v[42:45], v147, v147 op_sel_hi:[0,0,0]
	v_mfma_scale_f32_16x16x128_f8f6f4 v[204:207], v[172:179], v[212:219], v[38:41], v147, v147 op_sel_hi:[0,0,0]
	v_mfma_scale_f32_16x16x128_f8f6f4 v[208:211], v[180:187], v[212:219], v[34:37], v147, v147 op_sel_hi:[0,0,0]
	s_setprio 0
	s_barrier
	s_nop 4
	ds_read_b128 v[34:37], v154 offset:16384
	ds_read_b128 v[38:41], v154 offset:17408
	ds_read_b128 v[42:45], v154 offset:18432
	ds_read_b128 v[46:49], v154 offset:19456
	ds_read_b128 v[50:53], v154 offset:20480
	ds_read_b128 v[54:57], v154 offset:21504
	ds_read_b128 v[58:61], v154 offset:22528
	ds_read_b128 v[62:65], v154 offset:23552
	s_mov_b32 s41, m0
	s_mov_b32 m0, s16
	s_nop 0
	global_load_lds_dwordx4 v148, s[54:55]
	s_mov_b32 m0, s41
	s_add_u32 s88, s54, 0x40000
	s_mov_b32 s41, m0
	s_mov_b32 m0, s30
	s_nop 0
	global_load_lds_dwordx4 v150, s[54:55]
	s_mov_b32 m0, s41
	s_addc_u32 s89, s55, 0
	s_mov_b32 s41, m0
	s_mov_b32 m0, s31
	s_nop 0
	global_load_lds_dwordx4 v148, s[88:89]
	s_mov_b32 m0, s41
	s_nop 0
	s_mov_b32 s41, m0
	s_mov_b32 m0, s43
	s_nop 0
	global_load_lds_dwordx4 v150, s[88:89]
	s_mov_b32 m0, s41
	s_nop 0
	s_mov_b32 s41, m0
	s_mov_b32 m0, s14
	s_nop 0
	global_load_lds_dwordx4 v138, s[56:57]
	s_mov_b32 m0, s41
	s_nop 0
	s_mov_b32 s41, m0
	s_mov_b32 m0, s85
	s_nop 0
	global_load_lds_dwordx4 v149, s[56:57]
	s_mov_b32 m0, s41
	s_waitcnt vmcnt(8)
	s_waitcnt lgkmcnt(0)
	s_barrier
	s_setprio 1
	v_mfma_scale_f32_16x16x128_f8f6f4 v[94:97], v[156:163], v[34:41], v[94:97], v147, v147 op_sel_hi:[0,0,0]
	v_mfma_scale_f32_16x16x128_f8f6f4 v[90:93], v[164:171], v[34:41], v[90:93], v147, v147 op_sel_hi:[0,0,0]
	v_mfma_scale_f32_16x16x128_f8f6f4 v[86:89], v[156:163], v[42:49], v[86:89], v147, v147 op_sel_hi:[0,0,0]
	v_mfma_scale_f32_16x16x128_f8f6f4 v[82:85], v[164:171], v[42:49], v[82:85], v147, v147 op_sel_hi:[0,0,0]
	v_mfma_scale_f32_16x16x128_f8f6f4 v[78:81], v[156:163], v[50:57], v[78:81], v147, v147 op_sel_hi:[0,0,0]
	v_mfma_scale_f32_16x16x128_f8f6f4 v[74:77], v[164:171], v[50:57], v[74:77], v147, v147 op_sel_hi:[0,0,0]
	v_mfma_scale_f32_16x16x128_f8f6f4 v[212:215], v[156:163], v[58:65], v[70:73], v147, v147 op_sel_hi:[0,0,0]
	v_mfma_scale_f32_16x16x128_f8f6f4 v[216:219], v[164:171], v[58:65], v[66:69], v147, v147 op_sel_hi:[0,0,0]
	s_setprio 0
	s_setprio 1
	v_mfma_scale_f32_16x16x128_f8f6f4 v[220:223], v[172:179], v[34:41], v[30:33], v147, v147 op_sel_hi:[0,0,0]
	v_mfma_scale_f32_16x16x128_f8f6f4 v[224:227], v[180:187], v[34:41], v[26:29], v147, v147 op_sel_hi:[0,0,0]
	v_mfma_scale_f32_16x16x128_f8f6f4 v[228:231], v[172:179], v[42:49], v[22:25], v147, v147 op_sel_hi:[0,0,0]
	v_mfma_scale_f32_16x16x128_f8f6f4 v[232:235], v[180:187], v[42:49], v[18:21], v147, v147 op_sel_hi:[0,0,0]
	v_mfma_scale_f32_16x16x128_f8f6f4 v[236:239], v[172:179], v[50:57], v[14:17], v147, v147 op_sel_hi:[0,0,0]
	v_mfma_scale_f32_16x16x128_f8f6f4 v[240:243], v[180:187], v[50:57], v[10:13], v147, v147 op_sel_hi:[0,0,0]
	v_mfma_scale_f32_16x16x128_f8f6f4 v[244:247], v[172:179], v[58:65], v[6:9], v147, v147 op_sel_hi:[0,0,0]
	v_mfma_scale_f32_16x16x128_f8f6f4 v[248:251], v[180:187], v[58:65], v[2:5], v147, v147 op_sel_hi:[0,0,0]
	s_setprio 0
	s_barrier
; #define PG8_STAGE_A(bufoff, gbase, h) do { _Pragma("unroll") for (int _i = 0; _i < 2; ++_i) PG8_GLDS(gbase, va[(h) * 2 + _i], ldsb + (bufoff) + ldsw + _i * 8192); } while (0)
; #define PG8_STAGE_B(bufoff, gbase) do { _Pragma("unroll") for (int _i = 0; _i < 2; ++_i) PG8_GLDS(gbase, voffB[_i], ldsb + (bufoff) + ldsw + _i * 8192); } while (0)
; #define PG8_LDA(dst, b, h) do { _Pragma("unroll") for (int m = 0; m < 4; ++m) _Pragma("unroll") for (int k = 0; k < 2; ++k) dst[m][k] = *(const LAS i32x4*)(lds + PG8_SA(b, h) + aoff + m * 2048 + k * 1024); } while (0)
; #define PG8_LDB(dst, b, h) do { _Pragma("unroll") for (int n = 0; n < 2; ++n) _Pragma("unroll") for (int k = 0; k < 2; ++k) dst[n][k] = *(const LAS i32x4*)(lds + PG8_SB(b, h) + boff + n * 2048 + k * 1024); } while (0)
; #define PG8_WAIT_V(n) asm volatile("s_waitcnt vmcnt(" #n ")" ::: "memory")
; #define PG8_WAIT_L(n) asm volatile("s_waitcnt lgkmcnt(" #n ")" ::: "memory")
; #define PG8_BAR __builtin_amdgcn_s_barrier()
; #define PG8_SCHED __builtin_amdgcn_sched_barrier(0)
; template <class Epi, class Sched>
; __device__ __forceinline__ void gemm_phase(LAS unsigned char* lds, const Sched& S, const Epi& E) {
;     ...
;             PG8_LDB(B0, 1, 0); PG8_LDB(B1, 1, 1); PG8_SCHED; PG8_LDA(At, 1, 0); PG8_STAGE_A(PG8_SA(0, 1), a2, 1);
;             PG8_WAIT_V(8); PG8_WAIT_L(0); PG8_BAR; PG8_MMA(0, 0, At, B0); PG8_MMA(0, 1, At, B1); PG8_BAR; PG8_SCHED;
;             PG8_LDA(At, 1, 1); PG8_STAGE_B(PG8_SB(1, 0), b3); PG8_STAGE_B(PG8_SB(1, 1), b3 + HSTEP); PG8_STAGE_A(PG8_SA(1, 0), a3, 0);
;             PG8_WAIT_V(8); PG8_WAIT_L(0); PG8_BAR; PG8_MMA(1, 0, At, B0); PG8_MMA(1, 1, At, B1); PG8_BAR; PG8_SCHED;
;         }
	s_nop 1
	v_add_u32_e32 v14, 0x18000, v153
	v_add_u32_e32 v18, 0x1c000, v153
	s_nop 0
	ds_read_b128 v[2:5], v14
	ds_read_b128 v[6:9], v14 offset:1024
	ds_read_b128 v[10:13], v14 offset:2048
	ds_read_b128 v[14:17], v14 offset:3072
	ds_read_b128 v[156:159], v18
	ds_read_b128 v[160:163], v18 offset:1024
	ds_read_b128 v[164:167], v18 offset:2048
	ds_read_b128 v[168:171], v18 offset:3072
	ds_read_b128 v[18:21], v154 offset:32768
	ds_read_b128 v[22:25], v154 offset:33792
	ds_read_b128 v[26:29], v154 offset:34816
	ds_read_b128 v[30:33], v154 offset:35840
	ds_read_b128 v[34:37], v154 offset:36864
	ds_read_b128 v[38:41], v154 offset:37888
	ds_read_b128 v[66:69], v154 offset:38912
	ds_read_b128 v[70:73], v154 offset:39936
	s_mov_b32 s41, m0
	s_mov_b32 m0, s77
	s_nop 0
	global_load_lds_dwordx4 v151, s[56:57]
	s_mov_b32 m0, s41
	s_nop 0
	s_mov_b32 s41, m0
	s_mov_b32 m0, s79
	s_nop 0
	global_load_lds_dwordx4 v152, s[56:57]
	s_mov_b32 m0, s41
	s_waitcnt vmcnt(8)
	s_waitcnt lgkmcnt(0)
	s_barrier
	s_setprio 1
	v_mfma_scale_f32_16x16x128_f8f6f4 v[130:133], v[2:9], v[18:25], v[122:125], v147, v147 op_sel_hi:[0,0,0]
	v_mfma_scale_f32_16x16x128_f8f6f4 v[126:129], v[10:17], v[18:25], v[126:129], v147, v147 op_sel_hi:[0,0,0]
	v_mfma_scale_f32_16x16x128_f8f6f4 v[118:121], v[2:9], v[26:33], v[118:121], v147, v147 op_sel_hi:[0,0,0]
	v_mfma_scale_f32_16x16x128_f8f6f4 v[114:117], v[10:17], v[26:33], v[114:117], v147, v147 op_sel_hi:[0,0,0]
	v_mfma_scale_f32_16x16x128_f8f6f4 v[110:113], v[2:9], v[34:41], v[110:113], v147, v147 op_sel_hi:[0,0,0]
	v_mfma_scale_f32_16x16x128_f8f6f4 v[106:109], v[10:17], v[34:41], v[106:109], v147, v147 op_sel_hi:[0,0,0]
	v_mfma_scale_f32_16x16x128_f8f6f4 v[102:105], v[2:9], v[66:73], v[102:105], v147, v147 op_sel_hi:[0,0,0]
	v_mfma_scale_f32_16x16x128_f8f6f4 v[98:101], v[10:17], v[66:73], v[98:101], v147, v147 op_sel_hi:[0,0,0]
	s_setprio 0
	s_setprio 1
	v_mfma_scale_f32_16x16x128_f8f6f4 v[62:65], v[156:163], v[18:25], v[134:137], v147, v147 op_sel_hi:[0,0,0]
	v_mfma_scale_f32_16x16x128_f8f6f4 v[58:61], v[164:171], v[18:25], v[142:145], v147, v147 op_sel_hi:[0,0,0]
	v_mfma_scale_f32_16x16x128_f8f6f4 v[54:57], v[156:163], v[26:33], v[188:191], v147, v147 op_sel_hi:[0,0,0]
	v_mfma_scale_f32_16x16x128_f8f6f4 v[50:53], v[164:171], v[26:33], v[192:195], v147, v147 op_sel_hi:[0,0,0]
	v_mfma_scale_f32_16x16x128_f8f6f4 v[46:49], v[156:163], v[34:41], v[196:199], v147, v147 op_sel_hi:[0,0,0]
	v_mfma_scale_f32_16x16x128_f8f6f4 v[42:45], v[164:171], v[34:41], v[200:203], v147, v147 op_sel_hi:[0,0,0]
	v_mfma_scale_f32_16x16x128_f8f6f4 v[38:41], v[156:163], v[66:73], v[204:207], v147, v147 op_sel_hi:[0,0,0]
	v_mfma_scale_f32_16x16x128_f8f6f4 v[34:37], v[164:171], v[66:73], v[208:211], v147, v147 op_sel_hi:[0,0,0]
	s_setprio 0
	s_barrier
	ds_read_b128 v[18:21], v154 offset:49152
	ds_read_b128 v[22:25], v154 offset:50176
	ds_read_b128 v[172:175], v154 offset:51200
	ds_read_b128 v[176:179], v154 offset:52224
	ds_read_b128 v[180:183], v154 offset:53248
	ds_read_b128 v[184:187], v154 offset:54272
	ds_read_b128 v[188:191], v154 offset:55296
	ds_read_b128 v[192:195], v154 offset:56320
	s_mov_b32 s41, m0
	s_mov_b32 m0, s9
	s_nop 0
	global_load_lds_dwordx4 v148, s[44:45]
	s_mov_b32 m0, s41
	s_nop 0
	s_mov_b32 s41, m0
	s_mov_b32 m0, s96
	s_nop 0
	global_load_lds_dwordx4 v150, s[44:45]
	s_mov_b32 m0, s41
	s_add_u32 s44, s54, 0x40080
	s_addc_u32 s45, s55, 0
	s_mov_b32 s41, m0
	s_mov_b32 m0, s4
	s_nop 0
	global_load_lds_dwordx4 v148, s[44:45]
	s_mov_b32 m0, s41
	s_nop 0
	s_mov_b32 s41, m0
	s_mov_b32 m0, s5
	s_nop 0
	global_load_lds_dwordx4 v150, s[44:45]
	s_mov_b32 m0, s41
	s_nop 0
	s_mov_b32 s41, m0
	s_mov_b32 m0, s21
	s_nop 0
	global_load_lds_dwordx4 v138, s[52:53]
	s_mov_b32 m0, s41
	s_nop 0
	s_mov_b32 s41, m0
	s_mov_b32 m0, s82
	s_nop 0
	global_load_lds_dwordx4 v149, s[52:53]
	s_mov_b32 m0, s41
	s_waitcnt vmcnt(8)
	s_waitcnt lgkmcnt(0)
	s_barrier
	s_setprio 1
	v_mfma_scale_f32_16x16x128_f8f6f4 v[94:97], v[2:9], v[18:25], v[94:97], v147, v147 op_sel_hi:[0,0,0]
	v_mfma_scale_f32_16x16x128_f8f6f4 v[90:93], v[10:17], v[18:25], v[90:93], v147, v147 op_sel_hi:[0,0,0]
	v_mfma_scale_f32_16x16x128_f8f6f4 v[86:89], v[2:9], v[172:179], v[86:89], v147, v147 op_sel_hi:[0,0,0]
	v_mfma_scale_f32_16x16x128_f8f6f4 v[82:85], v[10:17], v[172:179], v[82:85], v147, v147 op_sel_hi:[0,0,0]
	v_mfma_scale_f32_16x16x128_f8f6f4 v[78:81], v[2:9], v[180:187], v[78:81], v147, v147 op_sel_hi:[0,0,0]
	v_mfma_scale_f32_16x16x128_f8f6f4 v[74:77], v[10:17], v[180:187], v[74:77], v147, v147 op_sel_hi:[0,0,0]
	v_mfma_scale_f32_16x16x128_f8f6f4 v[70:73], v[2:9], v[188:195], v[212:215], v147, v147 op_sel_hi:[0,0,0]
	v_mfma_scale_f32_16x16x128_f8f6f4 v[66:69], v[10:17], v[188:195], v[216:219], v147, v147 op_sel_hi:[0,0,0]
	s_setprio 0
	s_setprio 1
	v_mfma_scale_f32_16x16x128_f8f6f4 v[30:33], v[156:163], v[18:25], v[220:223], v147, v147 op_sel_hi:[0,0,0]
	v_mfma_scale_f32_16x16x128_f8f6f4 v[26:29], v[164:171], v[18:25], v[224:227], v147, v147 op_sel_hi:[0,0,0]
	v_mfma_scale_f32_16x16x128_f8f6f4 v[22:25], v[156:163], v[172:179], v[228:231], v147, v147 op_sel_hi:[0,0,0]
	v_mfma_scale_f32_16x16x128_f8f6f4 v[18:21], v[164:171], v[172:179], v[232:235], v147, v147 op_sel_hi:[0,0,0]
	v_mfma_scale_f32_16x16x128_f8f6f4 v[14:17], v[156:163], v[180:187], v[236:239], v147, v147 op_sel_hi:[0,0,0]
	v_mfma_scale_f32_16x16x128_f8f6f4 v[10:13], v[164:171], v[180:187], v[240:243], v147, v147 op_sel_hi:[0,0,0]
	v_mfma_scale_f32_16x16x128_f8f6f4 v[6:9], v[156:163], v[188:195], v[244:247], v147, v147 op_sel_hi:[0,0,0]
	v_mfma_scale_f32_16x16x128_f8f6f4 v[2:5], v[164:171], v[188:195], v[248:251], v147, v147 op_sel_hi:[0,0,0]
	s_setprio 0
	s_barrier
	s_add_i32 s35, s35, 2
	s_add_u32 s27, s27, 0x100
	s_addc_u32 s29, s29, 0
	s_cmp_gt_u32 s35, 13
	s_mov_b64 s[44:45], s[48:49]
	s_cbranch_scc0 .LBB0_1464
	s_and_b64 vcc, exec, s[24:25]
	s_cbranch_vccz .LBB0_1467
	s_barrier
